# MoE consumer K-loops: last iteration peeled, 14 clamped dummy LDS-DMA prefetches per wave and their drain removed, counted waits re-derived
# speedup vs baseline: 1.0027x; 1.0027x over previous
; #define G_WAIT_V(n) asm volatile("s_waitcnt vmcnt(" #n ")" ::: "memory")
; #define G_WAIT_L(n) asm volatile("s_waitcnt lgkmcnt(" #n ")" ::: "memory")
; #define G_BAR do { asm volatile("" ::: "memory"); __builtin_amdgcn_s_barrier(); asm volatile("" ::: "memory"); } while (0)
; #define G_SCHED __builtin_amdgcn_sched_barrier(0)
; #define STG_A(b, h, kt) do { const unsigned char* _g = A + (size_t)KT_(kt) * ASTEP; \
;         dma16((const void*)(_g + (size_t)((h) * 128) * ROWB), ROWB ? aoff[0][0] : aoff[h][0], lds_u + SA_(b, h) + dma0); \
;         dma16((const void*)(_g + (size_t)((h) * 128 + 64) * ROWB), ROWB ? aoff[0][0] : aoff[h][1], lds_u + SA_(b, h) + dma1); } while (0)
; #define STG_B(b, h, kt) do { const unsigned char* _g = img + (size_t)KT_(kt) * 32768 + (h) * 16384; \
;         dma16((const void*)(_g + dma0), boffl, lds_u + SB_(b, h) + dma0); \
;         dma16((const void*)(_g + dma1), boffl, lds_u + SB_(b, h) + dma1); } while (0)
; #define LDA_(dst, b, h) do { _Pragma("unroll") for (int _m = 0; _m < 4; ++_m) { \
;         dst[_m].lo = *(LAS3 const i32x4d*)(ap0 + SA_(b, h) + _m * 2048); \
;         dst[_m].hi = *(LAS3 const i32x4d*)(ap1 + SA_(b, h) + _m * 2048); } } while (0)
;     ...
;     for (int t = 0; t < nt; t += 2) {
;         const int t1 = (t + 1 < nt) ? t + 1 : nt - 1, t2 = (t + 2 < nt) ? t + 2 : nt - 1, t3 = (t + 3 < nt) ? t + 3 : nt - 1;
;         LDBF(B0, 0, 0); G_SCHED; LDA_(At, 0, 0); STG_A(1, 1, t1);
;         G_WAIT_L(8); G_BAR; G_WAIT_L(0); MMAD(0, 0, At, B0); G_BAR; G_SCHED;
;         LDBF(B1, 0, 1); STG_B(0, 0, t2);
;         G_BAR; G_WAIT_L(0); MMAD(0, 1, At, B1); G_BAR;
;         LDA_(At, 0, 1); STG_A(0, 0, t2);
;         G_BAR; G_WAIT_L(0); MMAD(1, 0, At, B0); G_BAR; G_SCHED;
;         STG_B(0, 1, t2);
;         G_WAIT_V(6); G_BAR; MMAD(1, 1, At, B1); G_BAR;
;         LDBF(B0, 1, 0); G_SCHED; LDA_(At, 1, 0); STG_A(0, 1, t2);
;         G_WAIT_L(8); G_BAR; G_WAIT_L(0); MMAD(0, 0, At, B0); G_BAR; G_SCHED;
;         LDBF(B1, 1, 1); STG_B(1, 0, t3);
;         G_BAR; G_WAIT_L(0); MMAD(0, 1, At, B1); G_BAR;
;         LDA_(At, 1, 1); STG_A(1, 0, t3);
;         G_BAR; G_WAIT_L(0); MMAD(1, 0, At, B0); G_BAR; G_SCHED;
;         STG_B(1, 1, t3);
;         G_WAIT_V(6); G_BAR; MMAD(1, 1, At, B1); G_BAR;
.LBB0_470:
	s_add_i32 s25, vcc_hi, 2
	s_min_u32 s28, vcc_hi, 12
	s_add_u32 s68, s0, 0x80
	s_addc_u32 s69, s1, 0
	s_and_b32 s29, s25, 14
	s_cmp_lt_u32 vcc_hi, 14
	s_cselect_b32 s29, s29, 15
	s_lshl_b32 s30, s29, 15
	s_add_u32 s30, s4, s30
	s_addc_u32 s31, vcc_lo, 0
	s_add_u32 s70, s30, s91
	s_addc_u32 s71, s31, s93
	s_add_u32 s72, s30, s92
	s_addc_u32 s73, s31, s96
	s_lshl_b32 s29, s29, 7
	s_add_u32 s56, s62, s29
	s_addc_u32 s57, s63, 0
	s_add_u32 s29, s30, 0x4000
	s_addc_u32 s30, s31, 0
	s_add_u32 s58, s29, s91
	s_addc_u32 s59, s30, s93
	s_add_u32 s60, s29, s92
	s_addc_u32 s61, s30, s96
	s_add_i32 s28, s28, 3
	s_lshl_b32 s29, s28, 15
	s_add_u32 s29, s4, s29
	s_addc_u32 s30, vcc_lo, 0
	s_add_u32 s36, s29, s91
	s_addc_u32 s37, s30, s93
	s_add_u32 s54, s29, s92
	s_addc_u32 s55, s30, s96
	s_lshl_b32 s28, s28, 7
	s_add_u32 s34, s62, s28
	s_addc_u32 s35, s63, 0
	s_add_u32 s31, s29, 0x4000
	ds_read_b128 v[0:3], v157
	ds_read_b128 v[8:11], v157 offset:8192
	ds_read_b128 v[4:7], v158
	ds_read_b128 v[12:15], v158 offset:8192
	s_addc_u32 s74, s30, 0
	s_add_u32 s28, s31, s91
	s_addc_u32 s29, s74, s93
	s_add_u32 s30, s31, s92
	s_addc_u32 s31, s74, s96
	s_add_u32 s0, s0, 0x100
	s_addc_u32 s1, s1, 0
	s_cmp_gt_u32 vcc_hi, 11
	ds_read_b128 v[160:163], v155
	ds_read_b128 v[168:171], v155 offset:2048
	ds_read_b128 v[164:167], v156
	ds_read_b128 v[172:175], v156 offset:2048
	ds_read_b128 v[176:179], v155 offset:4096
	ds_read_b128 v[184:187], v155 offset:6144
	ds_read_b128 v[180:183], v156 offset:4096
	ds_read_b128 v[188:191], v156 offset:6144
	s_mov_b32 m0, s38
	s_nop 0
	global_load_lds_dwordx4 v153, s[68:69]
	s_nop 0
	s_mov_b32 m0, s39
	s_nop 0
	global_load_lds_dwordx4 v154, s[68:69]
	s_waitcnt lgkmcnt(8)
	s_waitcnt vmcnt(10)
	s_barrier
	s_waitcnt lgkmcnt(0)
	v_readlane_b32 s69, v255, 8
	s_setprio 1
	s_waitcnt lgkmcnt(5)
	v_mfma_scale_f32_16x16x128_f8f6f4 v[140:143], v[0:7], v[160:167], v[140:143], v147, v147 op_sel:[0,1,0] op_sel_hi:[0,0,0]
	v_mfma_scale_f32_16x16x128_f8f6f4 v[132:135], v[8:15], v[160:167], v[132:135], v147, v147 op_sel:[0,1,0] op_sel_hi:[0,0,0]
	s_waitcnt lgkmcnt(4)
	v_mfma_scale_f32_16x16x128_f8f6f4 v[124:127], v[0:7], v[168:175], v[124:127], v147, v147 op_sel:[0,1,0] op_sel_hi:[0,0,0]
	v_mfma_scale_f32_16x16x128_f8f6f4 v[116:119], v[8:15], v[168:175], v[116:119], v147, v147 op_sel:[0,1,0] op_sel_hi:[0,0,0]
	s_waitcnt lgkmcnt(1)
	v_mfma_scale_f32_16x16x128_f8f6f4 v[208:211], v[0:7], v[176:183], v[108:111], v147, v147 op_sel:[0,1,0] op_sel_hi:[0,0,0]
	v_mfma_scale_f32_16x16x128_f8f6f4 v[212:215], v[8:15], v[176:183], v[100:103], v147, v147 op_sel:[0,1,0] op_sel_hi:[0,0,0]
	s_waitcnt lgkmcnt(0)
	v_mfma_scale_f32_16x16x128_f8f6f4 v[216:219], v[0:7], v[184:191], v[92:95], v147, v147 op_sel:[0,1,0] op_sel_hi:[0,0,0]
	v_mfma_scale_f32_16x16x128_f8f6f4 v[220:223], v[8:15], v[184:191], v[84:87], v147, v147 op_sel:[0,1,0] op_sel_hi:[0,0,0]
	s_setprio 0
	s_barrier
	ds_read_b128 v[192:195], v157 offset:16384
	ds_read_b128 v[200:203], v157 offset:24576
	ds_read_b128 v[196:199], v158 offset:16384
	ds_read_b128 v[204:207], v158 offset:24576
	s_mov_b32 m0, s78
	s_nop 0
	global_load_lds_dwordx4 v159, s[70:71]
	v_readlane_b32 s71, v255, 9
	s_mov_b32 m0, s69
	s_nop 0
	global_load_lds_dwordx4 v159, s[72:73]
	s_waitcnt vmcnt(10)
	s_barrier
	s_waitcnt lgkmcnt(0)
	s_setprio 1
	s_waitcnt lgkmcnt(1)
	v_mfma_scale_f32_16x16x128_f8f6f4 v[136:139], v[192:199], v[160:167], v[136:139], v147, v147 op_sel:[0,1,0] op_sel_hi:[0,0,0]
	s_waitcnt lgkmcnt(0)
	v_mfma_scale_f32_16x16x128_f8f6f4 v[128:131], v[200:207], v[160:167], v[128:131], v147, v147 op_sel:[0,1,0] op_sel_hi:[0,0,0]
	v_mfma_scale_f32_16x16x128_f8f6f4 v[120:123], v[192:199], v[168:175], v[120:123], v147, v147 op_sel:[0,1,0] op_sel_hi:[0,0,0]
	v_mfma_scale_f32_16x16x128_f8f6f4 v[112:115], v[200:207], v[168:175], v[112:115], v147, v147 op_sel:[0,1,0] op_sel_hi:[0,0,0]
	v_mfma_scale_f32_16x16x128_f8f6f4 v[224:227], v[192:199], v[176:183], v[104:107], v147, v147 op_sel:[0,1,0] op_sel_hi:[0,0,0]
	v_mfma_scale_f32_16x16x128_f8f6f4 v[176:179], v[200:207], v[176:183], v[96:99], v147, v147 op_sel:[0,1,0] op_sel_hi:[0,0,0]
	v_mfma_scale_f32_16x16x128_f8f6f4 v[180:183], v[192:199], v[184:191], v[88:91], v147, v147 op_sel:[0,1,0] op_sel_hi:[0,0,0]
	v_mfma_scale_f32_16x16x128_f8f6f4 v[184:187], v[200:207], v[184:191], v[20:23], v147, v147 op_sel:[0,1,0] op_sel_hi:[0,0,0]
	s_setprio 0
	s_barrier
	ds_read_b128 v[80:83], v155 offset:16384
	s_nop 2
	ds_read_b128 v[88:91], v155 offset:18432
	ds_read_b128 v[84:87], v156 offset:16384
	ds_read_b128 v[92:95], v156 offset:18432
	ds_read_b128 v[96:99], v155 offset:20480
	ds_read_b128 v[104:107], v155 offset:22528
	ds_read_b128 v[100:103], v156 offset:20480
	ds_read_b128 v[108:111], v156 offset:22528
	s_mov_b32 m0, s94
	s_nop 0
	global_load_lds_dwordx4 v144, s[56:57]
	s_nop 0
	s_mov_b32 m0, s83
	s_nop 0
	global_load_lds_dwordx4 v152, s[56:57]
	s_barrier
	s_waitcnt lgkmcnt(0)
	s_setprio 1
	s_waitcnt lgkmcnt(5)
	v_mfma_scale_f32_16x16x128_f8f6f4 v[76:79], v[0:7], v[80:87], v[76:79], v147, v147 op_sel:[0,1,0] op_sel_hi:[0,0,0]
	v_mfma_scale_f32_16x16x128_f8f6f4 v[68:71], v[8:15], v[80:87], v[68:71], v147, v147 op_sel:[0,1,0] op_sel_hi:[0,0,0]
	s_waitcnt lgkmcnt(4)
	v_mfma_scale_f32_16x16x128_f8f6f4 v[60:63], v[0:7], v[88:95], v[60:63], v147, v147 op_sel:[0,1,0] op_sel_hi:[0,0,0]
	v_mfma_scale_f32_16x16x128_f8f6f4 v[52:55], v[8:15], v[88:95], v[52:55], v147, v147 op_sel:[0,1,0] op_sel_hi:[0,0,0]
	s_waitcnt lgkmcnt(0)
	v_mfma_scale_f32_16x16x128_f8f6f4 v[240:243], v[8:15], v[104:111], v[240:243], v147, v147 op_sel:[0,1,0] op_sel_hi:[0,0,0]
	v_mfma_scale_f32_16x16x128_f8f6f4 v[228:231], v[0:7], v[96:103], v[44:47], v147, v147 op_sel:[0,1,0] op_sel_hi:[0,0,0]
	v_mfma_scale_f32_16x16x128_f8f6f4 v[232:235], v[8:15], v[96:103], v[36:39], v147, v147 op_sel:[0,1,0] op_sel_hi:[0,0,0]
	v_mfma_scale_f32_16x16x128_f8f6f4 v[236:239], v[0:7], v[104:111], v[28:31], v147, v147 op_sel:[0,1,0] op_sel_hi:[0,0,0]
	s_setprio 0
	s_barrier
; #define G_WAIT_V(n) asm volatile("s_waitcnt vmcnt(" #n ")" ::: "memory")
; #define G_WAIT_L(n) asm volatile("s_waitcnt lgkmcnt(" #n ")" ::: "memory")
; #define G_BAR do { asm volatile("" ::: "memory"); __builtin_amdgcn_s_barrier(); asm volatile("" ::: "memory"); } while (0)
; #define G_SCHED __builtin_amdgcn_sched_barrier(0)
; #define STG_A(b, h, kt) do { const unsigned char* _g = A + (size_t)KT_(kt) * ASTEP; \
;         dma16((const void*)(_g + (size_t)((h) * 128) * ROWB), ROWB ? aoff[0][0] : aoff[h][0], lds_u + SA_(b, h) + dma0); \
;         dma16((const void*)(_g + (size_t)((h) * 128 + 64) * ROWB), ROWB ? aoff[0][0] : aoff[h][1], lds_u + SA_(b, h) + dma1); } while (0)
; #define STG_B(b, h, kt) do { const unsigned char* _g = img + (size_t)KT_(kt) * 32768 + (h) * 16384; \
;         dma16((const void*)(_g + dma0), boffl, lds_u + SB_(b, h) + dma0); \
;         dma16((const void*)(_g + dma1), boffl, lds_u + SB_(b, h) + dma1); } while (0)
; #define LDA_(dst, b, h) do { _Pragma("unroll") for (int _m = 0; _m < 4; ++_m) { \
;         dst[_m].lo = *(LAS3 const i32x4d*)(ap0 + SA_(b, h) + _m * 2048); \
;         dst[_m].hi = *(LAS3 const i32x4d*)(ap1 + SA_(b, h) + _m * 2048); } } while (0)
;     ...
;     for (int t = 0; t < nt; t += 2) {
;         const int t1 = (t + 1 < nt) ? t + 1 : nt - 1, t2 = (t + 2 < nt) ? t + 2 : nt - 1, t3 = (t + 3 < nt) ? t + 3 : nt - 1;
;         LDBF(B0, 0, 0); G_SCHED; LDA_(At, 0, 0); STG_A(1, 1, t1);
;         G_WAIT_L(8); G_BAR; G_WAIT_L(0); MMAD(0, 0, At, B0); G_BAR; G_SCHED;
;         LDBF(B1, 0, 1); STG_B(0, 0, t2);
;         G_BAR; G_WAIT_L(0); MMAD(0, 1, At, B1); G_BAR;
;         LDA_(At, 0, 1); STG_A(0, 0, t2);
;         G_BAR; G_WAIT_L(0); MMAD(1, 0, At, B0); G_BAR; G_SCHED;
;         STG_B(0, 1, t2);
;         G_WAIT_V(6); G_BAR; MMAD(1, 1, At, B1); G_BAR;
;         LDBF(B0, 1, 0); G_SCHED; LDA_(At, 1, 0); STG_A(0, 1, t2);
;         G_WAIT_L(8); G_BAR; G_WAIT_L(0); MMAD(0, 0, At, B0); G_BAR; G_SCHED;
;         LDBF(B1, 1, 1); STG_B(1, 0, t3);
;         G_BAR; G_WAIT_L(0); MMAD(0, 1, At, B1); G_BAR;
;         LDA_(At, 1, 1); STG_A(1, 0, t3);
;         G_BAR; G_WAIT_L(0); MMAD(1, 0, At, B0); G_BAR; G_SCHED;
;         STG_B(1, 1, t3);
;         G_WAIT_V(6); G_BAR; MMAD(1, 1, At, B1); G_BAR;
	s_mov_b32 m0, s82
	s_nop 0
	global_load_lds_dwordx4 v159, s[58:59]
	s_mov_b32 m0, s71
	s_nop 0
	global_load_lds_dwordx4 v159, s[60:61]
	s_waitcnt vmcnt(10)
	s_barrier
	v_readlane_b32 s68, v255, 11
	v_readlane_b32 s60, v255, 10
	s_setprio 1
	v_mfma_scale_f32_16x16x128_f8f6f4 v[72:75], v[192:199], v[80:87], v[72:75], v147, v147 op_sel:[0,1,0] op_sel_hi:[0,0,0]
	v_mfma_scale_f32_16x16x128_f8f6f4 v[64:67], v[200:207], v[80:87], v[64:67], v147, v147 op_sel:[0,1,0] op_sel_hi:[0,0,0]
	v_mfma_scale_f32_16x16x128_f8f6f4 v[56:59], v[192:199], v[88:95], v[56:59], v147, v147 op_sel:[0,1,0] op_sel_hi:[0,0,0]
	v_mfma_scale_f32_16x16x128_f8f6f4 v[48:51], v[200:207], v[88:95], v[48:51], v147, v147 op_sel:[0,1,0] op_sel_hi:[0,0,0]
	v_mfma_scale_f32_16x16x128_f8f6f4 v[244:247], v[192:199], v[96:103], v[40:43], v147, v147 op_sel:[0,1,0] op_sel_hi:[0,0,0]
	v_mfma_scale_f32_16x16x128_f8f6f4 v[248:251], v[200:207], v[96:103], v[32:35], v147, v147 op_sel:[0,1,0] op_sel_hi:[0,0,0]
	v_mfma_scale_f32_16x16x128_f8f6f4 v[148:151], v[192:199], v[104:111], v[24:27], v147, v147 op_sel:[0,1,0] op_sel_hi:[0,0,0]
	v_mfma_scale_f32_16x16x128_f8f6f4 v[80:83], v[200:207], v[104:111], v[16:19], v147, v147 op_sel:[0,1,0] op_sel_hi:[0,0,0]
	s_setprio 0
	s_barrier
	ds_read_b128 v[0:3], v157 offset:32768
	ds_read_b128 v[8:11], v157 offset:40960
	ds_read_b128 v[4:7], v158 offset:32768
	ds_read_b128 v[12:15], v158 offset:40960
	s_nop 0
	ds_read_b128 v[16:19], v155 offset:32768
	ds_read_b128 v[24:27], v155 offset:34816
	ds_read_b128 v[20:23], v156 offset:32768
	ds_read_b128 v[28:31], v156 offset:34816
	ds_read_b128 v[32:35], v155 offset:36864
	ds_read_b128 v[40:43], v155 offset:38912
	ds_read_b128 v[36:39], v156 offset:36864
	ds_read_b128 v[44:47], v156 offset:38912
	s_mov_b32 m0, s79
	s_nop 0
	global_load_lds_dwordx4 v153, s[56:57]
	s_nop 0
	s_mov_b32 m0, s89
	s_nop 0
	global_load_lds_dwordx4 v154, s[56:57]
	s_waitcnt lgkmcnt(8)
	s_waitcnt vmcnt(10)
	s_barrier
	s_waitcnt lgkmcnt(0)
	s_setprio 1
	s_waitcnt lgkmcnt(5)
	v_mfma_scale_f32_16x16x128_f8f6f4 v[140:143], v[0:7], v[16:23], v[140:143], v147, v147 op_sel:[0,1,0] op_sel_hi:[0,0,0]
	v_mfma_scale_f32_16x16x128_f8f6f4 v[132:135], v[8:15], v[16:23], v[132:135], v147, v147 op_sel:[0,1,0] op_sel_hi:[0,0,0]
	s_waitcnt lgkmcnt(4)
	v_mfma_scale_f32_16x16x128_f8f6f4 v[124:127], v[0:7], v[24:31], v[124:127], v147, v147 op_sel:[0,1,0] op_sel_hi:[0,0,0]
	v_mfma_scale_f32_16x16x128_f8f6f4 v[116:119], v[8:15], v[24:31], v[116:119], v147, v147 op_sel:[0,1,0] op_sel_hi:[0,0,0]
	s_waitcnt lgkmcnt(1)
	v_mfma_scale_f32_16x16x128_f8f6f4 v[108:111], v[0:7], v[32:39], v[208:211], v147, v147 op_sel:[0,1,0] op_sel_hi:[0,0,0]
	v_mfma_scale_f32_16x16x128_f8f6f4 v[100:103], v[8:15], v[32:39], v[212:215], v147, v147 op_sel:[0,1,0] op_sel_hi:[0,0,0]
	s_waitcnt lgkmcnt(0)
	v_mfma_scale_f32_16x16x128_f8f6f4 v[92:95], v[0:7], v[40:47], v[216:219], v147, v147 op_sel:[0,1,0] op_sel_hi:[0,0,0]
	v_mfma_scale_f32_16x16x128_f8f6f4 v[84:87], v[8:15], v[40:47], v[220:223], v147, v147 op_sel:[0,1,0] op_sel_hi:[0,0,0]
	s_setprio 0
	s_barrier
	ds_read_b128 v[160:163], v157 offset:49152
	ds_read_b128 v[168:171], v157 offset:57344
	ds_read_b128 v[164:167], v158 offset:49152
	ds_read_b128 v[172:175], v158 offset:57344
	s_mov_b32 m0, s60
	s_nop 0
	global_load_lds_dwordx4 v159, s[36:37]
	s_mov_b32 m0, s68
	s_nop 0
	global_load_lds_dwordx4 v159, s[54:55]
	s_waitcnt vmcnt(10)
	s_barrier
	s_waitcnt lgkmcnt(0)
	s_setprio 1
	s_waitcnt lgkmcnt(1)
	v_mfma_scale_f32_16x16x128_f8f6f4 v[136:139], v[160:167], v[16:23], v[136:139], v147, v147 op_sel:[0,1,0] op_sel_hi:[0,0,0]
	s_waitcnt lgkmcnt(0)
	v_mfma_scale_f32_16x16x128_f8f6f4 v[128:131], v[168:175], v[16:23], v[128:131], v147, v147 op_sel:[0,1,0] op_sel_hi:[0,0,0]
	v_mfma_scale_f32_16x16x128_f8f6f4 v[120:123], v[160:167], v[24:31], v[120:123], v147, v147 op_sel:[0,1,0] op_sel_hi:[0,0,0]
	v_mfma_scale_f32_16x16x128_f8f6f4 v[112:115], v[168:175], v[24:31], v[112:115], v147, v147 op_sel:[0,1,0] op_sel_hi:[0,0,0]
	v_mfma_scale_f32_16x16x128_f8f6f4 v[104:107], v[160:167], v[32:39], v[224:227], v147, v147 op_sel:[0,1,0] op_sel_hi:[0,0,0]
	v_mfma_scale_f32_16x16x128_f8f6f4 v[96:99], v[168:175], v[32:39], v[176:179], v147, v147 op_sel:[0,1,0] op_sel_hi:[0,0,0]
	v_mfma_scale_f32_16x16x128_f8f6f4 v[88:91], v[160:167], v[40:47], v[180:183], v147, v147 op_sel:[0,1,0] op_sel_hi:[0,0,0]
	v_mfma_scale_f32_16x16x128_f8f6f4 v[20:23], v[168:175], v[40:47], v[184:187], v147, v147 op_sel:[0,1,0] op_sel_hi:[0,0,0]
	s_setprio 0
	s_barrier
	s_nop 2
	ds_read_b128 v[176:179], v155 offset:49152
	s_nop 0
	ds_read_b128 v[184:187], v155 offset:51200
	ds_read_b128 v[180:183], v156 offset:49152
	ds_read_b128 v[188:191], v156 offset:51200
	ds_read_b128 v[192:195], v155 offset:53248
	ds_read_b128 v[200:203], v155 offset:55296
	ds_read_b128 v[196:199], v156 offset:53248
	ds_read_b128 v[204:207], v156 offset:55296
	s_mov_b32 m0, s90
	s_nop 0
	global_load_lds_dwordx4 v144, s[34:35]
	s_nop 0
	s_mov_b32 m0, s88
	s_nop 0
	global_load_lds_dwordx4 v152, s[34:35]
	s_barrier
	s_waitcnt lgkmcnt(0)
	s_setprio 1
	s_waitcnt lgkmcnt(5)
	v_mfma_scale_f32_16x16x128_f8f6f4 v[76:79], v[0:7], v[176:183], v[76:79], v147, v147 op_sel:[0,1,0] op_sel_hi:[0,0,0]
	v_mfma_scale_f32_16x16x128_f8f6f4 v[68:71], v[8:15], v[176:183], v[68:71], v147, v147 op_sel:[0,1,0] op_sel_hi:[0,0,0]
	s_waitcnt lgkmcnt(4)
	v_mfma_scale_f32_16x16x128_f8f6f4 v[60:63], v[0:7], v[184:191], v[60:63], v147, v147 op_sel:[0,1,0] op_sel_hi:[0,0,0]
	v_mfma_scale_f32_16x16x128_f8f6f4 v[52:55], v[8:15], v[184:191], v[52:55], v147, v147 op_sel:[0,1,0] op_sel_hi:[0,0,0]
	s_waitcnt lgkmcnt(1)
	v_mfma_scale_f32_16x16x128_f8f6f4 v[44:47], v[0:7], v[192:199], v[228:231], v147, v147 op_sel:[0,1,0] op_sel_hi:[0,0,0]
	v_mfma_scale_f32_16x16x128_f8f6f4 v[36:39], v[8:15], v[192:199], v[232:235], v147, v147 op_sel:[0,1,0] op_sel_hi:[0,0,0]
	s_waitcnt lgkmcnt(0)
	v_mfma_scale_f32_16x16x128_f8f6f4 v[28:31], v[0:7], v[200:207], v[236:239], v147, v147 op_sel:[0,1,0] op_sel_hi:[0,0,0]
	v_mfma_scale_f32_16x16x128_f8f6f4 v[240:243], v[8:15], v[200:207], v[240:243], v147, v147 op_sel:[0,1,0] op_sel_hi:[0,0,0]
	s_setprio 0
	s_barrier
; #define G_WAIT_V(n) asm volatile("s_waitcnt vmcnt(" #n ")" ::: "memory")
; #define G_WAIT_L(n) asm volatile("s_waitcnt lgkmcnt(" #n ")" ::: "memory")
; #define G_BAR do { asm volatile("" ::: "memory"); __builtin_amdgcn_s_barrier(); asm volatile("" ::: "memory"); } while (0)
; #define G_SCHED __builtin_amdgcn_sched_barrier(0)
; #define STG_A(b, h, kt) do { const unsigned char* _g = A + (size_t)KT_(kt) * ASTEP; \
;         dma16((const void*)(_g + (size_t)((h) * 128) * ROWB), ROWB ? aoff[0][0] : aoff[h][0], lds_u + SA_(b, h) + dma0); \
;         dma16((const void*)(_g + (size_t)((h) * 128 + 64) * ROWB), ROWB ? aoff[0][0] : aoff[h][1], lds_u + SA_(b, h) + dma1); } while (0)
; #define STG_B(b, h, kt) do { const unsigned char* _g = img + (size_t)KT_(kt) * 32768 + (h) * 16384; \
;         dma16((const void*)(_g + dma0), boffl, lds_u + SB_(b, h) + dma0); \
;         dma16((const void*)(_g + dma1), boffl, lds_u + SB_(b, h) + dma1); } while (0)
; #define LDA_(dst, b, h) do { _Pragma("unroll") for (int _m = 0; _m < 4; ++_m) { \
;         dst[_m].lo = *(LAS3 const i32x4d*)(ap0 + SA_(b, h) + _m * 2048); \
;         dst[_m].hi = *(LAS3 const i32x4d*)(ap1 + SA_(b, h) + _m * 2048); } } while (0)
;     ...
;     for (int t = 0; t < nt; t += 2) {
;         const int t1 = (t + 1 < nt) ? t + 1 : nt - 1, t2 = (t + 2 < nt) ? t + 2 : nt - 1, t3 = (t + 3 < nt) ? t + 3 : nt - 1;
;         LDBF(B0, 0, 0); G_SCHED; LDA_(At, 0, 0); STG_A(1, 1, t1);
;         G_WAIT_L(8); G_BAR; G_WAIT_L(0); MMAD(0, 0, At, B0); G_BAR; G_SCHED;
;         LDBF(B1, 0, 1); STG_B(0, 0, t2);
;         G_BAR; G_WAIT_L(0); MMAD(0, 1, At, B1); G_BAR;
;         LDA_(At, 0, 1); STG_A(0, 0, t2);
;         G_BAR; G_WAIT_L(0); MMAD(1, 0, At, B0); G_BAR; G_SCHED;
;         STG_B(0, 1, t2);
;         G_WAIT_V(6); G_BAR; MMAD(1, 1, At, B1); G_BAR;
;         LDBF(B0, 1, 0); G_SCHED; LDA_(At, 1, 0); STG_A(0, 1, t2);
;         G_WAIT_L(8); G_BAR; G_WAIT_L(0); MMAD(0, 0, At, B0); G_BAR; G_SCHED;
;         LDBF(B1, 1, 1); STG_B(1, 0, t3);
;         G_BAR; G_WAIT_L(0); MMAD(0, 1, At, B1); G_BAR;
;         LDA_(At, 1, 1); STG_A(1, 0, t3);
;         G_BAR; G_WAIT_L(0); MMAD(1, 0, At, B0); G_BAR; G_SCHED;
;         STG_B(1, 1, t3);
;         G_WAIT_V(6); G_BAR; MMAD(1, 1, At, B1); G_BAR;
	s_mov_b32 m0, s33
	s_nop 0
	global_load_lds_dwordx4 v159, s[28:29]
	s_mov_b32 m0, s6
	s_nop 0
	global_load_lds_dwordx4 v159, s[30:31]
	s_waitcnt vmcnt(10)
	s_barrier
	s_setprio 1
	v_mfma_scale_f32_16x16x128_f8f6f4 v[72:75], v[160:167], v[176:183], v[72:75], v147, v147 op_sel:[0,1,0] op_sel_hi:[0,0,0]
	v_mfma_scale_f32_16x16x128_f8f6f4 v[64:67], v[168:175], v[176:183], v[64:67], v147, v147 op_sel:[0,1,0] op_sel_hi:[0,0,0]
	v_mfma_scale_f32_16x16x128_f8f6f4 v[56:59], v[160:167], v[184:191], v[56:59], v147, v147 op_sel:[0,1,0] op_sel_hi:[0,0,0]
	v_mfma_scale_f32_16x16x128_f8f6f4 v[48:51], v[168:175], v[184:191], v[48:51], v147, v147 op_sel:[0,1,0] op_sel_hi:[0,0,0]
	v_mfma_scale_f32_16x16x128_f8f6f4 v[40:43], v[160:167], v[192:199], v[244:247], v147, v147 op_sel:[0,1,0] op_sel_hi:[0,0,0]
	v_mfma_scale_f32_16x16x128_f8f6f4 v[32:35], v[168:175], v[192:199], v[248:251], v147, v147 op_sel:[0,1,0] op_sel_hi:[0,0,0]
	v_mfma_scale_f32_16x16x128_f8f6f4 v[24:27], v[160:167], v[200:207], v[148:151], v147, v147 op_sel:[0,1,0] op_sel_hi:[0,0,0]
	v_mfma_scale_f32_16x16x128_f8f6f4 v[16:19], v[168:175], v[200:207], v[80:83], v147, v147 op_sel:[0,1,0] op_sel_hi:[0,0,0]
	s_setprio 0
	s_barrier
	s_mov_b32 vcc_hi, s25
	s_cbranch_scc0 .LBB0_470
	s_add_i32 s25, vcc_hi, 2
	s_min_u32 s28, vcc_hi, 12
	s_add_u32 s68, s0, 0x80
	s_addc_u32 s69, s1, 0
	s_and_b32 s29, s25, 14
	s_cmp_lt_u32 vcc_hi, 14
	s_cselect_b32 s29, s29, 15
	s_lshl_b32 s30, s29, 15
	s_add_u32 s30, s4, s30
	s_addc_u32 s31, vcc_lo, 0
	s_add_u32 s70, s30, s91
	s_addc_u32 s71, s31, s93
	s_add_u32 s72, s30, s92
	s_addc_u32 s73, s31, s96
	s_lshl_b32 s29, s29, 7
	s_add_u32 s56, s62, s29
	s_addc_u32 s57, s63, 0
	s_add_u32 s29, s30, 0x4000
	s_addc_u32 s30, s31, 0
	s_add_u32 s58, s29, s91
	s_addc_u32 s59, s30, s93
	s_add_u32 s60, s29, s92
	s_addc_u32 s61, s30, s96
	s_add_i32 s28, s28, 3
	s_lshl_b32 s29, s28, 15
	s_add_u32 s29, s4, s29
	s_addc_u32 s30, vcc_lo, 0
	s_add_u32 s36, s29, s91
	s_addc_u32 s37, s30, s93
	s_add_u32 s54, s29, s92
	s_addc_u32 s55, s30, s96
	s_lshl_b32 s28, s28, 7
	s_add_u32 s34, s62, s28
	s_addc_u32 s35, s63, 0
	s_add_u32 s31, s29, 0x4000
	ds_read_b128 v[0:3], v157
	ds_read_b128 v[8:11], v157 offset:8192
	ds_read_b128 v[4:7], v158
	ds_read_b128 v[12:15], v158 offset:8192
	s_addc_u32 s74, s30, 0
	s_add_u32 s28, s31, s91
	s_addc_u32 s29, s74, s93
	s_add_u32 s30, s31, s92
	s_addc_u32 s31, s74, s96
	s_add_u32 s0, s0, 0x100
	s_addc_u32 s1, s1, 0
	s_cmp_gt_u32 vcc_hi, 13
	ds_read_b128 v[160:163], v155
	ds_read_b128 v[168:171], v155 offset:2048
	ds_read_b128 v[164:167], v156
	ds_read_b128 v[172:175], v156 offset:2048
	ds_read_b128 v[176:179], v155 offset:4096
	ds_read_b128 v[184:187], v155 offset:6144
	ds_read_b128 v[180:183], v156 offset:4096
	ds_read_b128 v[188:191], v156 offset:6144
	s_mov_b32 m0, s38
	s_nop 0
	global_load_lds_dwordx4 v153, s[68:69]
	s_nop 0
	s_mov_b32 m0, s39
	s_nop 0
	global_load_lds_dwordx4 v154, s[68:69]
	s_waitcnt lgkmcnt(8)
	s_waitcnt vmcnt(10)
	s_barrier
	s_waitcnt lgkmcnt(0)
	v_readlane_b32 s69, v255, 8
	s_setprio 1
	s_waitcnt lgkmcnt(5)
	v_mfma_scale_f32_16x16x128_f8f6f4 v[140:143], v[0:7], v[160:167], v[140:143], v147, v147 op_sel:[0,1,0] op_sel_hi:[0,0,0]
	v_mfma_scale_f32_16x16x128_f8f6f4 v[132:135], v[8:15], v[160:167], v[132:135], v147, v147 op_sel:[0,1,0] op_sel_hi:[0,0,0]
	s_waitcnt lgkmcnt(4)
	v_mfma_scale_f32_16x16x128_f8f6f4 v[124:127], v[0:7], v[168:175], v[124:127], v147, v147 op_sel:[0,1,0] op_sel_hi:[0,0,0]
	v_mfma_scale_f32_16x16x128_f8f6f4 v[116:119], v[8:15], v[168:175], v[116:119], v147, v147 op_sel:[0,1,0] op_sel_hi:[0,0,0]
	s_waitcnt lgkmcnt(1)
	v_mfma_scale_f32_16x16x128_f8f6f4 v[208:211], v[0:7], v[176:183], v[108:111], v147, v147 op_sel:[0,1,0] op_sel_hi:[0,0,0]
	v_mfma_scale_f32_16x16x128_f8f6f4 v[212:215], v[8:15], v[176:183], v[100:103], v147, v147 op_sel:[0,1,0] op_sel_hi:[0,0,0]
	s_waitcnt lgkmcnt(0)
	v_mfma_scale_f32_16x16x128_f8f6f4 v[216:219], v[0:7], v[184:191], v[92:95], v147, v147 op_sel:[0,1,0] op_sel_hi:[0,0,0]
	v_mfma_scale_f32_16x16x128_f8f6f4 v[220:223], v[8:15], v[184:191], v[84:87], v147, v147 op_sel:[0,1,0] op_sel_hi:[0,0,0]
	s_setprio 0
	s_barrier
	ds_read_b128 v[192:195], v157 offset:16384
	ds_read_b128 v[200:203], v157 offset:24576
	ds_read_b128 v[196:199], v158 offset:16384
	ds_read_b128 v[204:207], v158 offset:24576
	v_readlane_b32 s71, v255, 9
	s_waitcnt vmcnt(8)
	s_barrier
	s_waitcnt lgkmcnt(0)
	s_setprio 1
	s_waitcnt lgkmcnt(1)
	v_mfma_scale_f32_16x16x128_f8f6f4 v[136:139], v[192:199], v[160:167], v[136:139], v147, v147 op_sel:[0,1,0] op_sel_hi:[0,0,0]
	s_waitcnt lgkmcnt(0)
	v_mfma_scale_f32_16x16x128_f8f6f4 v[128:131], v[200:207], v[160:167], v[128:131], v147, v147 op_sel:[0,1,0] op_sel_hi:[0,0,0]
	v_mfma_scale_f32_16x16x128_f8f6f4 v[120:123], v[192:199], v[168:175], v[120:123], v147, v147 op_sel:[0,1,0] op_sel_hi:[0,0,0]
	v_mfma_scale_f32_16x16x128_f8f6f4 v[112:115], v[200:207], v[168:175], v[112:115], v147, v147 op_sel:[0,1,0] op_sel_hi:[0,0,0]
	v_mfma_scale_f32_16x16x128_f8f6f4 v[224:227], v[192:199], v[176:183], v[104:107], v147, v147 op_sel:[0,1,0] op_sel_hi:[0,0,0]
	v_mfma_scale_f32_16x16x128_f8f6f4 v[176:179], v[200:207], v[176:183], v[96:99], v147, v147 op_sel:[0,1,0] op_sel_hi:[0,0,0]
	v_mfma_scale_f32_16x16x128_f8f6f4 v[180:183], v[192:199], v[184:191], v[88:91], v147, v147 op_sel:[0,1,0] op_sel_hi:[0,0,0]
	v_mfma_scale_f32_16x16x128_f8f6f4 v[184:187], v[200:207], v[184:191], v[20:23], v147, v147 op_sel:[0,1,0] op_sel_hi:[0,0,0]
	s_setprio 0
	s_barrier
; #define G_WAIT_V(n) asm volatile("s_waitcnt vmcnt(" #n ")" ::: "memory")
; #define G_WAIT_L(n) asm volatile("s_waitcnt lgkmcnt(" #n ")" ::: "memory")
; #define G_BAR do { asm volatile("" ::: "memory"); __builtin_amdgcn_s_barrier(); asm volatile("" ::: "memory"); } while (0)
; #define G_SCHED __builtin_amdgcn_sched_barrier(0)
; #define STG_A(b, h, kt) do { const unsigned char* _g = A + (size_t)KT_(kt) * ASTEP; \
;         dma16((const void*)(_g + (size_t)((h) * 128) * ROWB), ROWB ? aoff[0][0] : aoff[h][0], lds_u + SA_(b, h) + dma0); \
;         dma16((const void*)(_g + (size_t)((h) * 128 + 64) * ROWB), ROWB ? aoff[0][0] : aoff[h][1], lds_u + SA_(b, h) + dma1); } while (0)
; #define STG_B(b, h, kt) do { const unsigned char* _g = img + (size_t)KT_(kt) * 32768 + (h) * 16384; \
;         dma16((const void*)(_g + dma0), boffl, lds_u + SB_(b, h) + dma0); \
;         dma16((const void*)(_g + dma1), boffl, lds_u + SB_(b, h) + dma1); } while (0)
; #define LDA_(dst, b, h) do { _Pragma("unroll") for (int _m = 0; _m < 4; ++_m) { \
;         dst[_m].lo = *(LAS3 const i32x4d*)(ap0 + SA_(b, h) + _m * 2048); \
;         dst[_m].hi = *(LAS3 const i32x4d*)(ap1 + SA_(b, h) + _m * 2048); } } while (0)
;     ...
;     for (int t = 0; t < nt; t += 2) {
;         const int t1 = (t + 1 < nt) ? t + 1 : nt - 1, t2 = (t + 2 < nt) ? t + 2 : nt - 1, t3 = (t + 3 < nt) ? t + 3 : nt - 1;
;         LDBF(B0, 0, 0); G_SCHED; LDA_(At, 0, 0); STG_A(1, 1, t1);
;         G_WAIT_L(8); G_BAR; G_WAIT_L(0); MMAD(0, 0, At, B0); G_BAR; G_SCHED;
;         LDBF(B1, 0, 1); STG_B(0, 0, t2);
;         G_BAR; G_WAIT_L(0); MMAD(0, 1, At, B1); G_BAR;
;         LDA_(At, 0, 1); STG_A(0, 0, t2);
;         G_BAR; G_WAIT_L(0); MMAD(1, 0, At, B0); G_BAR; G_SCHED;
;         STG_B(0, 1, t2);
;         G_WAIT_V(6); G_BAR; MMAD(1, 1, At, B1); G_BAR;
;         LDBF(B0, 1, 0); G_SCHED; LDA_(At, 1, 0); STG_A(0, 1, t2);
;         G_WAIT_L(8); G_BAR; G_WAIT_L(0); MMAD(0, 0, At, B0); G_BAR; G_SCHED;
;         LDBF(B1, 1, 1); STG_B(1, 0, t3);
;         G_BAR; G_WAIT_L(0); MMAD(0, 1, At, B1); G_BAR;
;         LDA_(At, 1, 1); STG_A(1, 0, t3);
;         G_BAR; G_WAIT_L(0); MMAD(1, 0, At, B0); G_BAR; G_SCHED;
;         STG_B(1, 1, t3);
;         G_WAIT_V(6); G_BAR; MMAD(1, 1, At, B1); G_BAR;
	ds_read_b128 v[80:83], v155 offset:16384
	s_nop 2
	ds_read_b128 v[88:91], v155 offset:18432
	ds_read_b128 v[84:87], v156 offset:16384
	ds_read_b128 v[92:95], v156 offset:18432
	ds_read_b128 v[96:99], v155 offset:20480
	ds_read_b128 v[104:107], v155 offset:22528
	ds_read_b128 v[100:103], v156 offset:20480
	ds_read_b128 v[108:111], v156 offset:22528
	s_nop 0
	s_barrier
	s_waitcnt lgkmcnt(0)
	s_setprio 1
	s_waitcnt lgkmcnt(5)
	v_mfma_scale_f32_16x16x128_f8f6f4 v[76:79], v[0:7], v[80:87], v[76:79], v147, v147 op_sel:[0,1,0] op_sel_hi:[0,0,0]
	v_mfma_scale_f32_16x16x128_f8f6f4 v[68:71], v[8:15], v[80:87], v[68:71], v147, v147 op_sel:[0,1,0] op_sel_hi:[0,0,0]
	s_waitcnt lgkmcnt(4)
	v_mfma_scale_f32_16x16x128_f8f6f4 v[60:63], v[0:7], v[88:95], v[60:63], v147, v147 op_sel:[0,1,0] op_sel_hi:[0,0,0]
	v_mfma_scale_f32_16x16x128_f8f6f4 v[52:55], v[8:15], v[88:95], v[52:55], v147, v147 op_sel:[0,1,0] op_sel_hi:[0,0,0]
	s_waitcnt lgkmcnt(0)
	v_mfma_scale_f32_16x16x128_f8f6f4 v[240:243], v[8:15], v[104:111], v[240:243], v147, v147 op_sel:[0,1,0] op_sel_hi:[0,0,0]
	v_mfma_scale_f32_16x16x128_f8f6f4 v[228:231], v[0:7], v[96:103], v[44:47], v147, v147 op_sel:[0,1,0] op_sel_hi:[0,0,0]
	v_mfma_scale_f32_16x16x128_f8f6f4 v[232:235], v[8:15], v[96:103], v[36:39], v147, v147 op_sel:[0,1,0] op_sel_hi:[0,0,0]
	v_mfma_scale_f32_16x16x128_f8f6f4 v[236:239], v[0:7], v[104:111], v[28:31], v147, v147 op_sel:[0,1,0] op_sel_hi:[0,0,0]
	s_setprio 0
	s_barrier
	s_waitcnt vmcnt(4)
	s_barrier
	v_readlane_b32 s68, v255, 11
	v_readlane_b32 s60, v255, 10
	s_setprio 1
	v_mfma_scale_f32_16x16x128_f8f6f4 v[72:75], v[192:199], v[80:87], v[72:75], v147, v147 op_sel:[0,1,0] op_sel_hi:[0,0,0]
	v_mfma_scale_f32_16x16x128_f8f6f4 v[64:67], v[200:207], v[80:87], v[64:67], v147, v147 op_sel:[0,1,0] op_sel_hi:[0,0,0]
	v_mfma_scale_f32_16x16x128_f8f6f4 v[56:59], v[192:199], v[88:95], v[56:59], v147, v147 op_sel:[0,1,0] op_sel_hi:[0,0,0]
	v_mfma_scale_f32_16x16x128_f8f6f4 v[48:51], v[200:207], v[88:95], v[48:51], v147, v147 op_sel:[0,1,0] op_sel_hi:[0,0,0]
	v_mfma_scale_f32_16x16x128_f8f6f4 v[244:247], v[192:199], v[96:103], v[40:43], v147, v147 op_sel:[0,1,0] op_sel_hi:[0,0,0]
	v_mfma_scale_f32_16x16x128_f8f6f4 v[248:251], v[200:207], v[96:103], v[32:35], v147, v147 op_sel:[0,1,0] op_sel_hi:[0,0,0]
	v_mfma_scale_f32_16x16x128_f8f6f4 v[148:151], v[192:199], v[104:111], v[24:27], v147, v147 op_sel:[0,1,0] op_sel_hi:[0,0,0]
	v_mfma_scale_f32_16x16x128_f8f6f4 v[80:83], v[200:207], v[104:111], v[16:19], v147, v147 op_sel:[0,1,0] op_sel_hi:[0,0,0]
	s_setprio 0
	s_barrier
	ds_read_b128 v[0:3], v157 offset:32768
	ds_read_b128 v[8:11], v157 offset:40960
	ds_read_b128 v[4:7], v158 offset:32768
	ds_read_b128 v[12:15], v158 offset:40960
	s_nop 0
	ds_read_b128 v[16:19], v155 offset:32768
	ds_read_b128 v[24:27], v155 offset:34816
	ds_read_b128 v[20:23], v156 offset:32768
	ds_read_b128 v[28:31], v156 offset:34816
	ds_read_b128 v[32:35], v155 offset:36864
	ds_read_b128 v[40:43], v155 offset:38912
	ds_read_b128 v[36:39], v156 offset:36864
	ds_read_b128 v[44:47], v156 offset:38912
	s_nop 0
	s_waitcnt lgkmcnt(8)
	s_waitcnt vmcnt(2)
	s_barrier
	s_waitcnt lgkmcnt(0)
	s_setprio 1
	s_waitcnt lgkmcnt(5)
	v_mfma_scale_f32_16x16x128_f8f6f4 v[140:143], v[0:7], v[16:23], v[140:143], v147, v147 op_sel:[0,1,0] op_sel_hi:[0,0,0]
	v_mfma_scale_f32_16x16x128_f8f6f4 v[132:135], v[8:15], v[16:23], v[132:135], v147, v147 op_sel:[0,1,0] op_sel_hi:[0,0,0]
	s_waitcnt lgkmcnt(4)
	v_mfma_scale_f32_16x16x128_f8f6f4 v[124:127], v[0:7], v[24:31], v[124:127], v147, v147 op_sel:[0,1,0] op_sel_hi:[0,0,0]
	v_mfma_scale_f32_16x16x128_f8f6f4 v[116:119], v[8:15], v[24:31], v[116:119], v147, v147 op_sel:[0,1,0] op_sel_hi:[0,0,0]
	s_waitcnt lgkmcnt(1)
	v_mfma_scale_f32_16x16x128_f8f6f4 v[108:111], v[0:7], v[32:39], v[208:211], v147, v147 op_sel:[0,1,0] op_sel_hi:[0,0,0]
	v_mfma_scale_f32_16x16x128_f8f6f4 v[100:103], v[8:15], v[32:39], v[212:215], v147, v147 op_sel:[0,1,0] op_sel_hi:[0,0,0]
	s_waitcnt lgkmcnt(0)
	v_mfma_scale_f32_16x16x128_f8f6f4 v[92:95], v[0:7], v[40:47], v[216:219], v147, v147 op_sel:[0,1,0] op_sel_hi:[0,0,0]
	v_mfma_scale_f32_16x16x128_f8f6f4 v[84:87], v[8:15], v[40:47], v[220:223], v147, v147 op_sel:[0,1,0] op_sel_hi:[0,0,0]
	s_setprio 0
	s_barrier
; #define G_WAIT_V(n) asm volatile("s_waitcnt vmcnt(" #n ")" ::: "memory")
; #define G_WAIT_L(n) asm volatile("s_waitcnt lgkmcnt(" #n ")" ::: "memory")
; #define G_BAR do { asm volatile("" ::: "memory"); __builtin_amdgcn_s_barrier(); asm volatile("" ::: "memory"); } while (0)
; #define G_SCHED __builtin_amdgcn_sched_barrier(0)
; #define STG_A(b, h, kt) do { const unsigned char* _g = A + (size_t)KT_(kt) * ASTEP; \
;         dma16((const void*)(_g + (size_t)((h) * 128) * ROWB), ROWB ? aoff[0][0] : aoff[h][0], lds_u + SA_(b, h) + dma0); \
;         dma16((const void*)(_g + (size_t)((h) * 128 + 64) * ROWB), ROWB ? aoff[0][0] : aoff[h][1], lds_u + SA_(b, h) + dma1); } while (0)
; #define STG_B(b, h, kt) do { const unsigned char* _g = img + (size_t)KT_(kt) * 32768 + (h) * 16384; \
;         dma16((const void*)(_g + dma0), boffl, lds_u + SB_(b, h) + dma0); \
;         dma16((const void*)(_g + dma1), boffl, lds_u + SB_(b, h) + dma1); } while (0)
; #define LDA_(dst, b, h) do { _Pragma("unroll") for (int _m = 0; _m < 4; ++_m) { \
;         dst[_m].lo = *(LAS3 const i32x4d*)(ap0 + SA_(b, h) + _m * 2048); \
;         dst[_m].hi = *(LAS3 const i32x4d*)(ap1 + SA_(b, h) + _m * 2048); } } while (0)
;     ...
;     for (int t = 0; t < nt; t += 2) {
;         const int t1 = (t + 1 < nt) ? t + 1 : nt - 1, t2 = (t + 2 < nt) ? t + 2 : nt - 1, t3 = (t + 3 < nt) ? t + 3 : nt - 1;
;         LDBF(B0, 0, 0); G_SCHED; LDA_(At, 0, 0); STG_A(1, 1, t1);
;         G_WAIT_L(8); G_BAR; G_WAIT_L(0); MMAD(0, 0, At, B0); G_BAR; G_SCHED;
;         LDBF(B1, 0, 1); STG_B(0, 0, t2);
;         G_BAR; G_WAIT_L(0); MMAD(0, 1, At, B1); G_BAR;
;         LDA_(At, 0, 1); STG_A(0, 0, t2);
;         G_BAR; G_WAIT_L(0); MMAD(1, 0, At, B0); G_BAR; G_SCHED;
;         STG_B(0, 1, t2);
;         G_WAIT_V(6); G_BAR; MMAD(1, 1, At, B1); G_BAR;
;         LDBF(B0, 1, 0); G_SCHED; LDA_(At, 1, 0); STG_A(0, 1, t2);
;         G_WAIT_L(8); G_BAR; G_WAIT_L(0); MMAD(0, 0, At, B0); G_BAR; G_SCHED;
;         LDBF(B1, 1, 1); STG_B(1, 0, t3);
;         G_BAR; G_WAIT_L(0); MMAD(0, 1, At, B1); G_BAR;
;         LDA_(At, 1, 1); STG_A(1, 0, t3);
;         G_BAR; G_WAIT_L(0); MMAD(1, 0, At, B0); G_BAR; G_SCHED;
;         STG_B(1, 1, t3);
;         G_WAIT_V(6); G_BAR; MMAD(1, 1, At, B1); G_BAR;
;     }
;     G_WAIT_V(0); G_WAIT_L(0);
;     { int wr0 = wid >> 2; asm volatile("" : "+s"(wr0)); if (wr0 == 0) G_BAR; }
;     G_BAR;
	ds_read_b128 v[160:163], v157 offset:49152
	ds_read_b128 v[168:171], v157 offset:57344
	ds_read_b128 v[164:167], v158 offset:49152
	ds_read_b128 v[172:175], v158 offset:57344
	s_waitcnt vmcnt(0)
	s_barrier
	s_waitcnt lgkmcnt(0)
	s_setprio 1
	s_waitcnt lgkmcnt(1)
	v_mfma_scale_f32_16x16x128_f8f6f4 v[136:139], v[160:167], v[16:23], v[136:139], v147, v147 op_sel:[0,1,0] op_sel_hi:[0,0,0]
	s_waitcnt lgkmcnt(0)
	v_mfma_scale_f32_16x16x128_f8f6f4 v[128:131], v[168:175], v[16:23], v[128:131], v147, v147 op_sel:[0,1,0] op_sel_hi:[0,0,0]
	v_mfma_scale_f32_16x16x128_f8f6f4 v[120:123], v[160:167], v[24:31], v[120:123], v147, v147 op_sel:[0,1,0] op_sel_hi:[0,0,0]
	v_mfma_scale_f32_16x16x128_f8f6f4 v[112:115], v[168:175], v[24:31], v[112:115], v147, v147 op_sel:[0,1,0] op_sel_hi:[0,0,0]
	v_mfma_scale_f32_16x16x128_f8f6f4 v[104:107], v[160:167], v[32:39], v[224:227], v147, v147 op_sel:[0,1,0] op_sel_hi:[0,0,0]
	v_mfma_scale_f32_16x16x128_f8f6f4 v[96:99], v[168:175], v[32:39], v[176:179], v147, v147 op_sel:[0,1,0] op_sel_hi:[0,0,0]
	v_mfma_scale_f32_16x16x128_f8f6f4 v[88:91], v[160:167], v[40:47], v[180:183], v147, v147 op_sel:[0,1,0] op_sel_hi:[0,0,0]
	v_mfma_scale_f32_16x16x128_f8f6f4 v[20:23], v[168:175], v[40:47], v[184:187], v147, v147 op_sel:[0,1,0] op_sel_hi:[0,0,0]
	s_setprio 0
	s_barrier
	s_nop 2
	ds_read_b128 v[176:179], v155 offset:49152
	s_nop 0
	ds_read_b128 v[184:187], v155 offset:51200
	ds_read_b128 v[180:183], v156 offset:49152
	ds_read_b128 v[188:191], v156 offset:51200
	ds_read_b128 v[192:195], v155 offset:53248
	ds_read_b128 v[200:203], v155 offset:55296
	ds_read_b128 v[196:199], v156 offset:53248
	ds_read_b128 v[204:207], v156 offset:55296
	s_nop 0
	s_barrier
	s_waitcnt lgkmcnt(0)
	s_setprio 1
	s_waitcnt lgkmcnt(5)
	v_mfma_scale_f32_16x16x128_f8f6f4 v[76:79], v[0:7], v[176:183], v[76:79], v147, v147 op_sel:[0,1,0] op_sel_hi:[0,0,0]
	v_mfma_scale_f32_16x16x128_f8f6f4 v[68:71], v[8:15], v[176:183], v[68:71], v147, v147 op_sel:[0,1,0] op_sel_hi:[0,0,0]
	s_waitcnt lgkmcnt(4)
	v_mfma_scale_f32_16x16x128_f8f6f4 v[60:63], v[0:7], v[184:191], v[60:63], v147, v147 op_sel:[0,1,0] op_sel_hi:[0,0,0]
	v_mfma_scale_f32_16x16x128_f8f6f4 v[52:55], v[8:15], v[184:191], v[52:55], v147, v147 op_sel:[0,1,0] op_sel_hi:[0,0,0]
	s_waitcnt lgkmcnt(1)
	v_mfma_scale_f32_16x16x128_f8f6f4 v[44:47], v[0:7], v[192:199], v[228:231], v147, v147 op_sel:[0,1,0] op_sel_hi:[0,0,0]
	v_mfma_scale_f32_16x16x128_f8f6f4 v[36:39], v[8:15], v[192:199], v[232:235], v147, v147 op_sel:[0,1,0] op_sel_hi:[0,0,0]
	s_waitcnt lgkmcnt(0)
	v_mfma_scale_f32_16x16x128_f8f6f4 v[28:31], v[0:7], v[200:207], v[236:239], v147, v147 op_sel:[0,1,0] op_sel_hi:[0,0,0]
	v_mfma_scale_f32_16x16x128_f8f6f4 v[240:243], v[8:15], v[200:207], v[240:243], v147, v147 op_sel:[0,1,0] op_sel_hi:[0,0,0]
	s_setprio 0
	s_barrier
	s_waitcnt vmcnt(0)
	s_barrier
	s_setprio 1
	v_mfma_scale_f32_16x16x128_f8f6f4 v[72:75], v[160:167], v[176:183], v[72:75], v147, v147 op_sel:[0,1,0] op_sel_hi:[0,0,0]
	v_mfma_scale_f32_16x16x128_f8f6f4 v[64:67], v[168:175], v[176:183], v[64:67], v147, v147 op_sel:[0,1,0] op_sel_hi:[0,0,0]
	v_mfma_scale_f32_16x16x128_f8f6f4 v[56:59], v[160:167], v[184:191], v[56:59], v147, v147 op_sel:[0,1,0] op_sel_hi:[0,0,0]
	v_mfma_scale_f32_16x16x128_f8f6f4 v[48:51], v[168:175], v[184:191], v[48:51], v147, v147 op_sel:[0,1,0] op_sel_hi:[0,0,0]
	v_mfma_scale_f32_16x16x128_f8f6f4 v[40:43], v[160:167], v[192:199], v[244:247], v147, v147 op_sel:[0,1,0] op_sel_hi:[0,0,0]
	v_mfma_scale_f32_16x16x128_f8f6f4 v[32:35], v[168:175], v[192:199], v[248:251], v147, v147 op_sel:[0,1,0] op_sel_hi:[0,0,0]
	v_mfma_scale_f32_16x16x128_f8f6f4 v[24:27], v[160:167], v[200:207], v[148:151], v147, v147 op_sel:[0,1,0] op_sel_hi:[0,0,0]
	v_mfma_scale_f32_16x16x128_f8f6f4 v[16:19], v[168:175], v[200:207], v[80:83], v147, v147 op_sel:[0,1,0] op_sel_hi:[0,0,0]
	s_setprio 0
	s_barrier
	s_mov_b32 vcc_hi, s25
	s_waitcnt vmcnt(0)
	s_waitcnt lgkmcnt(0)
	s_mov_b32 s0, s77
	s_mov_b32 s70, s82
	s_mov_b32 s72, s83
	s_mov_b32 s59, s89
	s_mov_b32 s61, s79
	s_cmp_eq_u32 s0, 0
	s_cbranch_scc0 .LBB0_473
	s_barrier

; #define G_WAIT_V(n) asm volatile("s_waitcnt vmcnt(" #n ")" ::: "memory")
; #define G_WAIT_L(n) asm volatile("s_waitcnt lgkmcnt(" #n ")" ::: "memory")
; #define G_BAR do { asm volatile("" ::: "memory"); __builtin_amdgcn_s_barrier(); asm volatile("" ::: "memory"); } while (0)
; #define G_SCHED __builtin_amdgcn_sched_barrier(0)
; #define STG_A(b, h, kt) do { const unsigned char* _g = A + (size_t)KT_(kt) * ASTEP; \
;         dma16((const void*)(_g + (size_t)((h) * 128) * ROWB), ROWB ? aoff[0][0] : aoff[h][0], lds_u + SA_(b, h) + dma0); \
;         dma16((const void*)(_g + (size_t)((h) * 128 + 64) * ROWB), ROWB ? aoff[0][0] : aoff[h][1], lds_u + SA_(b, h) + dma1); } while (0)
; #define STG_B(b, h, kt) do { const unsigned char* _g = img + (size_t)KT_(kt) * 32768 + (h) * 16384; \
;         dma16((const void*)(_g + dma0), boffl, lds_u + SB_(b, h) + dma0); \
;         dma16((const void*)(_g + dma1), boffl, lds_u + SB_(b, h) + dma1); } while (0)
; #define LDA_(dst, b, h) do { _Pragma("unroll") for (int _m = 0; _m < 4; ++_m) { \
;         dst[_m].lo = *(LAS3 const i32x4d*)(ap0 + SA_(b, h) + _m * 2048); \
;         dst[_m].hi = *(LAS3 const i32x4d*)(ap1 + SA_(b, h) + _m * 2048); } } while (0)
;     ...
;     for (int t = 0; t < nt; t += 2) {
;         const int t1 = (t + 1 < nt) ? t + 1 : nt - 1, t2 = (t + 2 < nt) ? t + 2 : nt - 1, t3 = (t + 3 < nt) ? t + 3 : nt - 1;
;         LDBF(B0, 0, 0); G_SCHED; LDA_(At, 0, 0); STG_A(1, 1, t1);
;         G_WAIT_L(8); G_BAR; G_WAIT_L(0); MMAD(0, 0, At, B0); G_BAR; G_SCHED;
;         LDBF(B1, 0, 1); STG_B(0, 0, t2);
;         G_BAR; G_WAIT_L(0); MMAD(0, 1, At, B1); G_BAR;
;         LDA_(At, 0, 1); STG_A(0, 0, t2);
;         G_BAR; G_WAIT_L(0); MMAD(1, 0, At, B0); G_BAR; G_SCHED;
;         STG_B(0, 1, t2);
;         G_WAIT_V(6); G_BAR; MMAD(1, 1, At, B1); G_BAR;
;         LDBF(B0, 1, 0); G_SCHED; LDA_(At, 1, 0); STG_A(0, 1, t2);
;         G_WAIT_L(8); G_BAR; G_WAIT_L(0); MMAD(0, 0, At, B0); G_BAR; G_SCHED;
;         LDBF(B1, 1, 1); STG_B(1, 0, t3);
;         G_BAR; G_WAIT_L(0); MMAD(0, 1, At, B1); G_BAR;
;         LDA_(At, 1, 1); STG_A(1, 0, t3);
;         G_BAR; G_WAIT_L(0); MMAD(1, 0, At, B0); G_BAR; G_SCHED;
;         STG_B(1, 1, t3);
;         G_WAIT_V(6); G_BAR; MMAD(1, 1, At, B1); G_BAR;
.LBB0_562:
	s_add_i32 vcc_lo, vcc_hi, 2
	s_add_u32 s30, s64, s0
	s_addc_u32 s31, s65, s1
	s_add_u32 s68, s30, 0xc000
	s_addc_u32 s69, s31, 0
	s_add_u32 s76, s30, 0xe000
	s_addc_u32 s77, s31, 0
	s_add_u32 s0, s0, 0x10000
	s_addc_u32 s1, s1, 0
	s_and_b32 s30, s0, 0x70000
	s_cmp_lt_u32 vcc_hi, 14
	s_cselect_b32 s30, s30, 0x78000
	s_add_u32 s31, s4, s30
	s_addc_u32 s34, s25, 0
	s_add_u32 s84, s31, s91
	s_addc_u32 s85, s34, s93
	s_add_u32 s80, s31, s92
	s_addc_u32 s81, s34, s96
	s_add_u32 s74, s64, s30
	s_addc_u32 s75, s65, 0
	s_add_u32 s72, s74, 0x2000
	s_addc_u32 s73, s75, 0
	s_add_u32 s30, s31, 0x4000
	s_addc_u32 s31, s34, 0
	s_add_u32 s70, s30, s91
	s_addc_u32 s71, s31, s93
	s_add_u32 s62, s30, s92
	s_addc_u32 s63, s31, s96
	s_add_u32 s60, s74, 0x4000
	s_addc_u32 s61, s75, 0
	s_add_u32 s58, s74, 0x6000
	s_addc_u32 s59, s75, 0
	s_min_u32 s30, vcc_hi, 12
	s_lshl_b32 s30, s30, 15
	s_add_i32 s30, s30, 0x18000
	s_and_b32 s30, s30, 0x78000
	s_add_u32 s31, s4, s30
	s_addc_u32 s34, s25, 0
	s_add_u32 s56, s31, s91
	s_addc_u32 s57, s34, s93
	s_add_u32 s54, s31, s92
	s_addc_u32 s55, s34, s96
	s_add_u32 s48, s64, s30
	s_addc_u32 s49, s65, 0
	s_add_u32 s36, s48, 0x2000
	ds_read_b128 v[0:3], v139
	ds_read_b128 v[148:151], v139 offset:8192
	ds_read_b128 v[4:7], v140
	ds_read_b128 v[152:155], v140 offset:8192
	s_addc_u32 s37, s49, 0
	s_add_u32 s30, s31, 0x4000
	s_addc_u32 s31, s34, 0
	s_add_u32 s34, s30, s91
	s_addc_u32 s35, s31, s93
	s_add_u32 s30, s30, s92
	s_addc_u32 s31, s31, s96
	s_cmp_gt_u32 vcc_hi, 11
	ds_read_b128 v[156:159], v137
	ds_read_b128 v[164:167], v137 offset:2048
	ds_read_b128 v[160:163], v138
	ds_read_b128 v[168:171], v138 offset:2048
	ds_read_b128 v[172:175], v137 offset:4096
	ds_read_b128 v[180:183], v137 offset:6144
	ds_read_b128 v[176:179], v138 offset:4096
	ds_read_b128 v[184:187], v138 offset:6144
	s_mov_b32 s39, s78
	s_mov_b32 m0, s40
	s_nop 0
	global_load_lds_dwordx4 v136, s[68:69]
	s_mov_b32 m0, s41
	s_nop 0
	global_load_lds_dwordx4 v136, s[76:77]
	s_waitcnt lgkmcnt(8)
	s_waitcnt vmcnt(10)
	s_barrier
	s_waitcnt lgkmcnt(0)
	v_readlane_b32 s69, v255, 8
	s_mov_b32 s78, s39
	s_setprio 1
	s_waitcnt lgkmcnt(5)
	v_mfma_scale_f32_16x16x128_f8f6f4 v[132:135], v[0:7], v[156:163], v[132:135], v144, v144 op_sel:[0,1,0] op_sel_hi:[0,0,0]
	s_waitcnt lgkmcnt(4)
	v_mfma_scale_f32_16x16x128_f8f6f4 v[116:119], v[148:155], v[164:171], v[116:119], v144, v144 op_sel:[0,1,0] op_sel_hi:[0,0,0]
	s_waitcnt lgkmcnt(1)
	v_mfma_scale_f32_16x16x128_f8f6f4 v[108:111], v[0:7], v[172:179], v[108:111], v144, v144 op_sel:[0,1,0] op_sel_hi:[0,0,0]
	v_mfma_scale_f32_16x16x128_f8f6f4 v[196:199], v[148:155], v[156:163], v[128:131], v144, v144 op_sel:[0,1,0] op_sel_hi:[0,0,0]
	v_mfma_scale_f32_16x16x128_f8f6f4 v[200:203], v[0:7], v[164:171], v[124:127], v144, v144 op_sel:[0,1,0] op_sel_hi:[0,0,0]
	v_mfma_scale_f32_16x16x128_f8f6f4 v[204:207], v[148:155], v[172:179], v[100:103], v144, v144 op_sel:[0,1,0] op_sel_hi:[0,0,0]
	s_waitcnt lgkmcnt(0)
	v_mfma_scale_f32_16x16x128_f8f6f4 v[208:211], v[0:7], v[180:187], v[92:95], v144, v144 op_sel:[0,1,0] op_sel_hi:[0,0,0]
	v_mfma_scale_f32_16x16x128_f8f6f4 v[212:215], v[148:155], v[180:187], v[84:87], v144, v144 op_sel:[0,1,0] op_sel_hi:[0,0,0]
	s_setprio 0
	s_barrier
	s_nop 0
	ds_read_b128 v[124:127], v139 offset:16384
	ds_read_b128 v[188:191], v139 offset:24576
	ds_read_b128 v[128:131], v140 offset:16384
	ds_read_b128 v[192:195], v140 offset:24576
	s_mov_b32 m0, s39
	s_nop 0
	global_load_lds_dwordx4 v141, s[84:85]
	s_nop 0
	s_mov_b32 m0, s69
	s_nop 0
	global_load_lds_dwordx4 v141, s[80:81]
	s_waitcnt vmcnt(10)
	s_barrier
	s_waitcnt lgkmcnt(0)
	s_setprio 1
	s_waitcnt lgkmcnt(1)
	v_mfma_scale_f32_16x16x128_f8f6f4 v[120:123], v[124:131], v[156:163], v[120:123], v144, v144 op_sel:[0,1,0] op_sel_hi:[0,0,0]
	s_waitcnt lgkmcnt(0)
	v_mfma_scale_f32_16x16x128_f8f6f4 v[112:115], v[188:195], v[156:163], v[112:115], v144, v144 op_sel:[0,1,0] op_sel_hi:[0,0,0]
	v_mfma_scale_f32_16x16x128_f8f6f4 v[104:107], v[124:131], v[164:171], v[104:107], v144, v144 op_sel:[0,1,0] op_sel_hi:[0,0,0]
	v_mfma_scale_f32_16x16x128_f8f6f4 v[164:167], v[188:195], v[164:171], v[96:99], v144, v144 op_sel:[0,1,0] op_sel_hi:[0,0,0]
	v_mfma_scale_f32_16x16x128_f8f6f4 v[168:171], v[124:131], v[172:179], v[88:91], v144, v144 op_sel:[0,1,0] op_sel_hi:[0,0,0]
	v_mfma_scale_f32_16x16x128_f8f6f4 v[172:175], v[188:195], v[172:179], v[80:83], v144, v144 op_sel:[0,1,0] op_sel_hi:[0,0,0]
	v_mfma_scale_f32_16x16x128_f8f6f4 v[176:179], v[124:131], v[180:187], v[76:79], v144, v144 op_sel:[0,1,0] op_sel_hi:[0,0,0]
	v_mfma_scale_f32_16x16x128_f8f6f4 v[180:183], v[188:195], v[180:187], v[72:75], v144, v144 op_sel:[0,1,0] op_sel_hi:[0,0,0]
	s_setprio 0
	s_barrier
	s_nop 4
	ds_read_b128 v[72:75], v137 offset:16384
	ds_read_b128 v[80:83], v137 offset:18432
	ds_read_b128 v[76:79], v138 offset:16384
	ds_read_b128 v[84:87], v138 offset:18432
	ds_read_b128 v[88:91], v137 offset:20480
	ds_read_b128 v[96:99], v137 offset:22528
	ds_read_b128 v[92:95], v138 offset:20480
	ds_read_b128 v[100:103], v138 offset:22528
	s_mov_b32 m0, s94
	s_nop 0
	global_load_lds_dwordx4 v136, s[74:75]
	s_nop 0
	s_mov_b32 m0, s83
	s_nop 0
	global_load_lds_dwordx4 v136, s[72:73]
	s_barrier
; #define G_WAIT_V(n) asm volatile("s_waitcnt vmcnt(" #n ")" ::: "memory")
; #define G_WAIT_L(n) asm volatile("s_waitcnt lgkmcnt(" #n ")" ::: "memory")
; #define G_BAR do { asm volatile("" ::: "memory"); __builtin_amdgcn_s_barrier(); asm volatile("" ::: "memory"); } while (0)
; #define G_SCHED __builtin_amdgcn_sched_barrier(0)
; #define STG_A(b, h, kt) do { const unsigned char* _g = A + (size_t)KT_(kt) * ASTEP; \
;         dma16((const void*)(_g + (size_t)((h) * 128) * ROWB), ROWB ? aoff[0][0] : aoff[h][0], lds_u + SA_(b, h) + dma0); \
;         dma16((const void*)(_g + (size_t)((h) * 128 + 64) * ROWB), ROWB ? aoff[0][0] : aoff[h][1], lds_u + SA_(b, h) + dma1); } while (0)
; #define STG_B(b, h, kt) do { const unsigned char* _g = img + (size_t)KT_(kt) * 32768 + (h) * 16384; \
;         dma16((const void*)(_g + dma0), boffl, lds_u + SB_(b, h) + dma0); \
;         dma16((const void*)(_g + dma1), boffl, lds_u + SB_(b, h) + dma1); } while (0)
; #define LDA_(dst, b, h) do { _Pragma("unroll") for (int _m = 0; _m < 4; ++_m) { \
;         dst[_m].lo = *(LAS3 const i32x4d*)(ap0 + SA_(b, h) + _m * 2048); \
;         dst[_m].hi = *(LAS3 const i32x4d*)(ap1 + SA_(b, h) + _m * 2048); } } while (0)
;     ...
;     for (int t = 0; t < nt; t += 2) {
;         const int t1 = (t + 1 < nt) ? t + 1 : nt - 1, t2 = (t + 2 < nt) ? t + 2 : nt - 1, t3 = (t + 3 < nt) ? t + 3 : nt - 1;
;         LDBF(B0, 0, 0); G_SCHED; LDA_(At, 0, 0); STG_A(1, 1, t1);
;         G_WAIT_L(8); G_BAR; G_WAIT_L(0); MMAD(0, 0, At, B0); G_BAR; G_SCHED;
;         LDBF(B1, 0, 1); STG_B(0, 0, t2);
;         G_BAR; G_WAIT_L(0); MMAD(0, 1, At, B1); G_BAR;
;         LDA_(At, 0, 1); STG_A(0, 0, t2);
;         G_BAR; G_WAIT_L(0); MMAD(1, 0, At, B0); G_BAR; G_SCHED;
;         STG_B(0, 1, t2);
;         G_WAIT_V(6); G_BAR; MMAD(1, 1, At, B1); G_BAR;
;         LDBF(B0, 1, 0); G_SCHED; LDA_(At, 1, 0); STG_A(0, 1, t2);
;         G_WAIT_L(8); G_BAR; G_WAIT_L(0); MMAD(0, 0, At, B0); G_BAR; G_SCHED;
;         LDBF(B1, 1, 1); STG_B(1, 0, t3);
;         G_BAR; G_WAIT_L(0); MMAD(0, 1, At, B1); G_BAR;
;         LDA_(At, 1, 1); STG_A(1, 0, t3);
;         G_BAR; G_WAIT_L(0); MMAD(1, 0, At, B0); G_BAR; G_SCHED;
;         STG_B(1, 1, t3);
;         G_WAIT_V(6); G_BAR; MMAD(1, 1, At, B1); G_BAR;
	s_waitcnt lgkmcnt(0)
	s_setprio 1
	s_waitcnt lgkmcnt(5)
	v_mfma_scale_f32_16x16x128_f8f6f4 v[68:71], v[0:7], v[72:79], v[68:71], v144, v144 op_sel:[0,1,0] op_sel_hi:[0,0,0]
	v_mfma_scale_f32_16x16x128_f8f6f4 v[64:67], v[148:155], v[72:79], v[64:67], v144, v144 op_sel:[0,1,0] op_sel_hi:[0,0,0]
	s_waitcnt lgkmcnt(4)
	v_mfma_scale_f32_16x16x128_f8f6f4 v[60:63], v[0:7], v[80:87], v[60:63], v144, v144 op_sel:[0,1,0] op_sel_hi:[0,0,0]
	v_mfma_scale_f32_16x16x128_f8f6f4 v[52:55], v[148:155], v[80:87], v[52:55], v144, v144 op_sel:[0,1,0] op_sel_hi:[0,0,0]
	s_waitcnt lgkmcnt(1)
	v_mfma_scale_f32_16x16x128_f8f6f4 v[216:219], v[0:7], v[88:95], v[44:47], v144, v144 op_sel:[0,1,0] op_sel_hi:[0,0,0]
	v_mfma_scale_f32_16x16x128_f8f6f4 v[220:223], v[148:155], v[88:95], v[40:43], v144, v144 op_sel:[0,1,0] op_sel_hi:[0,0,0]
	s_waitcnt lgkmcnt(0)
	v_mfma_scale_f32_16x16x128_f8f6f4 v[224:227], v[0:7], v[96:103], v[28:31], v144, v144 op_sel:[0,1,0] op_sel_hi:[0,0,0]
	v_mfma_scale_f32_16x16x128_f8f6f4 v[228:231], v[148:155], v[96:103], v[24:27], v144, v144 op_sel:[0,1,0] op_sel_hi:[0,0,0]
	s_setprio 0
	s_barrier
	s_mov_b32 m0, s82
	s_nop 0
	global_load_lds_dwordx4 v141, s[70:71]
	v_readlane_b32 s71, v255, 9
	s_mov_b32 m0, s71
	s_nop 0
	global_load_lds_dwordx4 v141, s[62:63]
	s_waitcnt vmcnt(10)
	s_barrier
	v_readlane_b32 s68, v255, 11
	s_setprio 1
	v_mfma_scale_f32_16x16x128_f8f6f4 v[56:59], v[124:131], v[72:79], v[56:59], v144, v144 op_sel:[0,1,0] op_sel_hi:[0,0,0]
	v_mfma_scale_f32_16x16x128_f8f6f4 v[48:51], v[188:195], v[72:79], v[48:51], v144, v144 op_sel:[0,1,0] op_sel_hi:[0,0,0]
	v_mfma_scale_f32_16x16x128_f8f6f4 v[232:235], v[124:131], v[80:87], v[36:39], v144, v144 op_sel:[0,1,0] op_sel_hi:[0,0,0]
	v_mfma_scale_f32_16x16x128_f8f6f4 v[236:239], v[188:195], v[80:87], v[32:35], v144, v144 op_sel:[0,1,0] op_sel_hi:[0,0,0]
	v_mfma_scale_f32_16x16x128_f8f6f4 v[240:243], v[124:131], v[88:95], v[20:23], v144, v144 op_sel:[0,1,0] op_sel_hi:[0,0,0]
	v_mfma_scale_f32_16x16x128_f8f6f4 v[244:247], v[188:195], v[88:95], v[16:19], v144, v144 op_sel:[0,1,0] op_sel_hi:[0,0,0]
	v_mfma_scale_f32_16x16x128_f8f6f4 v[248:251], v[124:131], v[96:103], v[12:15], v144, v144 op_sel:[0,1,0] op_sel_hi:[0,0,0]
	v_mfma_scale_f32_16x16x128_f8f6f4 v[188:191], v[188:195], v[96:103], v[8:11], v144, v144 op_sel:[0,1,0] op_sel_hi:[0,0,0]
	s_setprio 0
	s_barrier
	ds_read_b128 v[0:3], v139 offset:32768
	s_nop 3
	ds_read_b128 v[8:11], v139 offset:40960
	ds_read_b128 v[4:7], v140 offset:32768
	ds_read_b128 v[12:15], v140 offset:40960
	ds_read_b128 v[16:19], v137 offset:32768
	ds_read_b128 v[24:27], v137 offset:34816
	ds_read_b128 v[20:23], v138 offset:32768
	ds_read_b128 v[28:31], v138 offset:34816
	ds_read_b128 v[32:35], v137 offset:36864
	ds_read_b128 v[40:43], v137 offset:38912
	ds_read_b128 v[36:39], v138 offset:36864
	ds_read_b128 v[44:47], v138 offset:38912
	s_mov_b32 m0, s79
	s_nop 0
	global_load_lds_dwordx4 v136, s[60:61]
	s_mov_b32 m0, s89
	s_nop 0
	global_load_lds_dwordx4 v136, s[58:59]
	s_waitcnt lgkmcnt(8)
	s_waitcnt vmcnt(10)
	s_barrier
	s_waitcnt lgkmcnt(0)
	v_readlane_b32 s60, v255, 10
	s_setprio 1
	s_waitcnt lgkmcnt(5)
	v_mfma_scale_f32_16x16x128_f8f6f4 v[132:135], v[0:7], v[16:23], v[132:135], v144, v144 op_sel:[0,1,0] op_sel_hi:[0,0,0]
	v_mfma_scale_f32_16x16x128_f8f6f4 v[128:131], v[8:15], v[16:23], v[196:199], v144, v144 op_sel:[0,1,0] op_sel_hi:[0,0,0]
	s_waitcnt lgkmcnt(4)
	v_mfma_scale_f32_16x16x128_f8f6f4 v[124:127], v[0:7], v[24:31], v[200:203], v144, v144 op_sel:[0,1,0] op_sel_hi:[0,0,0]
	v_mfma_scale_f32_16x16x128_f8f6f4 v[116:119], v[8:15], v[24:31], v[116:119], v144, v144 op_sel:[0,1,0] op_sel_hi:[0,0,0]
	s_waitcnt lgkmcnt(1)
	v_mfma_scale_f32_16x16x128_f8f6f4 v[108:111], v[0:7], v[32:39], v[108:111], v144, v144 op_sel:[0,1,0] op_sel_hi:[0,0,0]
	v_mfma_scale_f32_16x16x128_f8f6f4 v[100:103], v[8:15], v[32:39], v[204:207], v144, v144 op_sel:[0,1,0] op_sel_hi:[0,0,0]
	s_waitcnt lgkmcnt(0)
	v_mfma_scale_f32_16x16x128_f8f6f4 v[92:95], v[0:7], v[40:47], v[208:211], v144, v144 op_sel:[0,1,0] op_sel_hi:[0,0,0]
	v_mfma_scale_f32_16x16x128_f8f6f4 v[84:87], v[8:15], v[40:47], v[212:215], v144, v144 op_sel:[0,1,0] op_sel_hi:[0,0,0]
	s_setprio 0
	s_barrier
	ds_read_b128 v[148:151], v139 offset:49152
	ds_read_b128 v[156:159], v139 offset:57344
	ds_read_b128 v[152:155], v140 offset:49152
	ds_read_b128 v[160:163], v140 offset:57344
	s_mov_b32 m0, s60
	s_nop 0
	global_load_lds_dwordx4 v141, s[56:57]
	s_mov_b32 m0, s68
	s_nop 0
	global_load_lds_dwordx4 v141, s[54:55]
	s_waitcnt vmcnt(10)
	s_barrier
	s_waitcnt lgkmcnt(0)
	s_setprio 1
	s_waitcnt lgkmcnt(1)
	v_mfma_scale_f32_16x16x128_f8f6f4 v[120:123], v[148:155], v[16:23], v[120:123], v144, v144 op_sel:[0,1,0] op_sel_hi:[0,0,0]
	s_waitcnt lgkmcnt(0)
	v_mfma_scale_f32_16x16x128_f8f6f4 v[112:115], v[156:163], v[16:23], v[112:115], v144, v144 op_sel:[0,1,0] op_sel_hi:[0,0,0]
	v_mfma_scale_f32_16x16x128_f8f6f4 v[104:107], v[148:155], v[24:31], v[104:107], v144, v144 op_sel:[0,1,0] op_sel_hi:[0,0,0]
	v_mfma_scale_f32_16x16x128_f8f6f4 v[96:99], v[156:163], v[24:31], v[164:167], v144, v144 op_sel:[0,1,0] op_sel_hi:[0,0,0]
	v_mfma_scale_f32_16x16x128_f8f6f4 v[88:91], v[148:155], v[32:39], v[168:171], v144, v144 op_sel:[0,1,0] op_sel_hi:[0,0,0]
	v_mfma_scale_f32_16x16x128_f8f6f4 v[80:83], v[156:163], v[32:39], v[172:175], v144, v144 op_sel:[0,1,0] op_sel_hi:[0,0,0]
	v_mfma_scale_f32_16x16x128_f8f6f4 v[76:79], v[148:155], v[40:47], v[176:179], v144, v144 op_sel:[0,1,0] op_sel_hi:[0,0,0]
	v_mfma_scale_f32_16x16x128_f8f6f4 v[72:75], v[156:163], v[40:47], v[180:183], v144, v144 op_sel:[0,1,0] op_sel_hi:[0,0,0]
	s_setprio 0
	s_barrier
; #define G_WAIT_V(n) asm volatile("s_waitcnt vmcnt(" #n ")" ::: "memory")
; #define G_WAIT_L(n) asm volatile("s_waitcnt lgkmcnt(" #n ")" ::: "memory")
; #define G_BAR do { asm volatile("" ::: "memory"); __builtin_amdgcn_s_barrier(); asm volatile("" ::: "memory"); } while (0)
; #define G_SCHED __builtin_amdgcn_sched_barrier(0)
; #define STG_A(b, h, kt) do { const unsigned char* _g = A + (size_t)KT_(kt) * ASTEP; \
;         dma16((const void*)(_g + (size_t)((h) * 128) * ROWB), ROWB ? aoff[0][0] : aoff[h][0], lds_u + SA_(b, h) + dma0); \
;         dma16((const void*)(_g + (size_t)((h) * 128 + 64) * ROWB), ROWB ? aoff[0][0] : aoff[h][1], lds_u + SA_(b, h) + dma1); } while (0)
; #define STG_B(b, h, kt) do { const unsigned char* _g = img + (size_t)KT_(kt) * 32768 + (h) * 16384; \
;         dma16((const void*)(_g + dma0), boffl, lds_u + SB_(b, h) + dma0); \
;         dma16((const void*)(_g + dma1), boffl, lds_u + SB_(b, h) + dma1); } while (0)
; #define LDA_(dst, b, h) do { _Pragma("unroll") for (int _m = 0; _m < 4; ++_m) { \
;         dst[_m].lo = *(LAS3 const i32x4d*)(ap0 + SA_(b, h) + _m * 2048); \
;         dst[_m].hi = *(LAS3 const i32x4d*)(ap1 + SA_(b, h) + _m * 2048); } } while (0)
;     ...
;     for (int t = 0; t < nt; t += 2) {
;         const int t1 = (t + 1 < nt) ? t + 1 : nt - 1, t2 = (t + 2 < nt) ? t + 2 : nt - 1, t3 = (t + 3 < nt) ? t + 3 : nt - 1;
;         LDBF(B0, 0, 0); G_SCHED; LDA_(At, 0, 0); STG_A(1, 1, t1);
;         G_WAIT_L(8); G_BAR; G_WAIT_L(0); MMAD(0, 0, At, B0); G_BAR; G_SCHED;
;         LDBF(B1, 0, 1); STG_B(0, 0, t2);
;         G_BAR; G_WAIT_L(0); MMAD(0, 1, At, B1); G_BAR;
;         LDA_(At, 0, 1); STG_A(0, 0, t2);
;         G_BAR; G_WAIT_L(0); MMAD(1, 0, At, B0); G_BAR; G_SCHED;
;         STG_B(0, 1, t2);
;         G_WAIT_V(6); G_BAR; MMAD(1, 1, At, B1); G_BAR;
;         LDBF(B0, 1, 0); G_SCHED; LDA_(At, 1, 0); STG_A(0, 1, t2);
;         G_WAIT_L(8); G_BAR; G_WAIT_L(0); MMAD(0, 0, At, B0); G_BAR; G_SCHED;
;         LDBF(B1, 1, 1); STG_B(1, 0, t3);
;         G_BAR; G_WAIT_L(0); MMAD(0, 1, At, B1); G_BAR;
;         LDA_(At, 1, 1); STG_A(1, 0, t3);
;         G_BAR; G_WAIT_L(0); MMAD(1, 0, At, B0); G_BAR; G_SCHED;
;         STG_B(1, 1, t3);
;         G_WAIT_V(6); G_BAR; MMAD(1, 1, At, B1); G_BAR;
	ds_read_b128 v[16:19], v137 offset:49152
	ds_read_b128 v[164:167], v137 offset:51200
	ds_read_b128 v[20:23], v138 offset:49152
	ds_read_b128 v[168:171], v138 offset:51200
	ds_read_b128 v[172:175], v137 offset:53248
	ds_read_b128 v[180:183], v137 offset:55296
	ds_read_b128 v[176:179], v138 offset:53248
	ds_read_b128 v[184:187], v138 offset:55296
	s_mov_b32 m0, s90
	s_nop 0
	global_load_lds_dwordx4 v136, s[48:49]
	s_mov_b32 m0, s88
	s_nop 0
	global_load_lds_dwordx4 v136, s[36:37]
	s_barrier
	s_waitcnt lgkmcnt(0)
	s_setprio 1
	s_waitcnt lgkmcnt(5)
	v_mfma_scale_f32_16x16x128_f8f6f4 v[68:71], v[0:7], v[16:23], v[68:71], v144, v144 op_sel:[0,1,0] op_sel_hi:[0,0,0]
	v_mfma_scale_f32_16x16x128_f8f6f4 v[64:67], v[8:15], v[16:23], v[64:67], v144, v144 op_sel:[0,1,0] op_sel_hi:[0,0,0]
	s_waitcnt lgkmcnt(4)
	v_mfma_scale_f32_16x16x128_f8f6f4 v[60:63], v[0:7], v[164:171], v[60:63], v144, v144 op_sel:[0,1,0] op_sel_hi:[0,0,0]
	v_mfma_scale_f32_16x16x128_f8f6f4 v[52:55], v[8:15], v[164:171], v[52:55], v144, v144 op_sel:[0,1,0] op_sel_hi:[0,0,0]
	s_waitcnt lgkmcnt(1)
	v_mfma_scale_f32_16x16x128_f8f6f4 v[44:47], v[0:7], v[172:179], v[216:219], v144, v144 op_sel:[0,1,0] op_sel_hi:[0,0,0]
	v_mfma_scale_f32_16x16x128_f8f6f4 v[40:43], v[8:15], v[172:179], v[220:223], v144, v144 op_sel:[0,1,0] op_sel_hi:[0,0,0]
	s_waitcnt lgkmcnt(0)
	v_mfma_scale_f32_16x16x128_f8f6f4 v[28:31], v[0:7], v[180:187], v[224:227], v144, v144 op_sel:[0,1,0] op_sel_hi:[0,0,0]
	v_mfma_scale_f32_16x16x128_f8f6f4 v[24:27], v[8:15], v[180:187], v[228:231], v144, v144 op_sel:[0,1,0] op_sel_hi:[0,0,0]
	s_setprio 0
	s_barrier
	s_mov_b32 m0, s33
	s_nop 0
	global_load_lds_dwordx4 v141, s[34:35]
	s_mov_b32 m0, s6
	s_nop 0
	global_load_lds_dwordx4 v141, s[30:31]
	s_waitcnt vmcnt(10)
	s_barrier
	s_setprio 1
	v_mfma_scale_f32_16x16x128_f8f6f4 v[56:59], v[148:155], v[16:23], v[56:59], v144, v144 op_sel:[0,1,0] op_sel_hi:[0,0,0]
	v_mfma_scale_f32_16x16x128_f8f6f4 v[48:51], v[156:163], v[16:23], v[48:51], v144, v144 op_sel:[0,1,0] op_sel_hi:[0,0,0]
	v_mfma_scale_f32_16x16x128_f8f6f4 v[36:39], v[148:155], v[164:171], v[232:235], v144, v144 op_sel:[0,1,0] op_sel_hi:[0,0,0]
	v_mfma_scale_f32_16x16x128_f8f6f4 v[32:35], v[156:163], v[164:171], v[236:239], v144, v144 op_sel:[0,1,0] op_sel_hi:[0,0,0]
	v_mfma_scale_f32_16x16x128_f8f6f4 v[20:23], v[148:155], v[172:179], v[240:243], v144, v144 op_sel:[0,1,0] op_sel_hi:[0,0,0]
	v_mfma_scale_f32_16x16x128_f8f6f4 v[16:19], v[156:163], v[172:179], v[244:247], v144, v144 op_sel:[0,1,0] op_sel_hi:[0,0,0]
	v_mfma_scale_f32_16x16x128_f8f6f4 v[12:15], v[148:155], v[180:187], v[248:251], v144, v144 op_sel:[0,1,0] op_sel_hi:[0,0,0]
	v_mfma_scale_f32_16x16x128_f8f6f4 v[8:11], v[156:163], v[180:187], v[188:191], v144, v144 op_sel:[0,1,0] op_sel_hi:[0,0,0]
	s_setprio 0
	s_barrier
	s_mov_b32 vcc_hi, vcc_lo
	s_cbranch_scc0 .LBB0_562
	s_add_i32 vcc_lo, vcc_hi, 2
	s_add_u32 s30, s64, s0
	s_addc_u32 s31, s65, s1
	s_add_u32 s68, s30, 0xc000
	s_addc_u32 s69, s31, 0
	s_add_u32 s76, s30, 0xe000
	s_addc_u32 s77, s31, 0
	s_add_u32 s0, s0, 0x10000
	s_addc_u32 s1, s1, 0
	s_and_b32 s30, s0, 0x70000
	s_cmp_lt_u32 vcc_hi, 14
	s_cselect_b32 s30, s30, 0x78000
	s_add_u32 s31, s4, s30
	s_addc_u32 s34, s25, 0
	s_add_u32 s84, s31, s91
	s_addc_u32 s85, s34, s93
	s_add_u32 s80, s31, s92
	s_addc_u32 s81, s34, s96
	s_add_u32 s74, s64, s30
	s_addc_u32 s75, s65, 0
	s_add_u32 s72, s74, 0x2000
	s_addc_u32 s73, s75, 0
	s_add_u32 s30, s31, 0x4000
	s_addc_u32 s31, s34, 0
	s_add_u32 s70, s30, s91
	s_addc_u32 s71, s31, s93
	s_add_u32 s62, s30, s92
	s_addc_u32 s63, s31, s96
	s_add_u32 s60, s74, 0x4000
	s_addc_u32 s61, s75, 0
	s_add_u32 s58, s74, 0x6000
	s_addc_u32 s59, s75, 0
	s_min_u32 s30, vcc_hi, 12
	s_lshl_b32 s30, s30, 15
	s_add_i32 s30, s30, 0x18000
	s_and_b32 s30, s30, 0x78000
	s_add_u32 s31, s4, s30
	s_addc_u32 s34, s25, 0
	s_add_u32 s56, s31, s91
	s_addc_u32 s57, s34, s93
	s_add_u32 s54, s31, s92
	s_addc_u32 s55, s34, s96
	s_add_u32 s48, s64, s30
	s_addc_u32 s49, s65, 0
	s_add_u32 s36, s48, 0x2000
	ds_read_b128 v[0:3], v139
	ds_read_b128 v[148:151], v139 offset:8192
	ds_read_b128 v[4:7], v140
	ds_read_b128 v[152:155], v140 offset:8192
	s_addc_u32 s37, s49, 0
	s_add_u32 s30, s31, 0x4000
	s_addc_u32 s31, s34, 0
	s_add_u32 s34, s30, s91
	s_addc_u32 s35, s31, s93
	s_add_u32 s30, s30, s92
	s_addc_u32 s31, s31, s96
	s_cmp_gt_u32 vcc_hi, 13
	ds_read_b128 v[156:159], v137
	ds_read_b128 v[164:167], v137 offset:2048
	ds_read_b128 v[160:163], v138
	ds_read_b128 v[168:171], v138 offset:2048
	ds_read_b128 v[172:175], v137 offset:4096
	ds_read_b128 v[180:183], v137 offset:6144
	ds_read_b128 v[176:179], v138 offset:4096
	ds_read_b128 v[184:187], v138 offset:6144
	s_mov_b32 s39, s78
	s_mov_b32 m0, s40
	s_nop 0
	global_load_lds_dwordx4 v136, s[68:69]
	s_mov_b32 m0, s41
	s_nop 0
	global_load_lds_dwordx4 v136, s[76:77]
	s_waitcnt lgkmcnt(8)
	s_waitcnt vmcnt(10)
	s_barrier
	s_waitcnt lgkmcnt(0)
	v_readlane_b32 s69, v255, 8
	s_mov_b32 s78, s39
	s_setprio 1
	s_waitcnt lgkmcnt(5)
	v_mfma_scale_f32_16x16x128_f8f6f4 v[132:135], v[0:7], v[156:163], v[132:135], v144, v144 op_sel:[0,1,0] op_sel_hi:[0,0,0]
	s_waitcnt lgkmcnt(4)
	v_mfma_scale_f32_16x16x128_f8f6f4 v[116:119], v[148:155], v[164:171], v[116:119], v144, v144 op_sel:[0,1,0] op_sel_hi:[0,0,0]
	s_waitcnt lgkmcnt(1)
	v_mfma_scale_f32_16x16x128_f8f6f4 v[108:111], v[0:7], v[172:179], v[108:111], v144, v144 op_sel:[0,1,0] op_sel_hi:[0,0,0]
	v_mfma_scale_f32_16x16x128_f8f6f4 v[196:199], v[148:155], v[156:163], v[128:131], v144, v144 op_sel:[0,1,0] op_sel_hi:[0,0,0]
	v_mfma_scale_f32_16x16x128_f8f6f4 v[200:203], v[0:7], v[164:171], v[124:127], v144, v144 op_sel:[0,1,0] op_sel_hi:[0,0,0]
	v_mfma_scale_f32_16x16x128_f8f6f4 v[204:207], v[148:155], v[172:179], v[100:103], v144, v144 op_sel:[0,1,0] op_sel_hi:[0,0,0]
	s_waitcnt lgkmcnt(0)
	v_mfma_scale_f32_16x16x128_f8f6f4 v[208:211], v[0:7], v[180:187], v[92:95], v144, v144 op_sel:[0,1,0] op_sel_hi:[0,0,0]
	v_mfma_scale_f32_16x16x128_f8f6f4 v[212:215], v[148:155], v[180:187], v[84:87], v144, v144 op_sel:[0,1,0] op_sel_hi:[0,0,0]
	s_setprio 0
	s_barrier
; #define G_WAIT_V(n) asm volatile("s_waitcnt vmcnt(" #n ")" ::: "memory")
; #define G_WAIT_L(n) asm volatile("s_waitcnt lgkmcnt(" #n ")" ::: "memory")
; #define G_BAR do { asm volatile("" ::: "memory"); __builtin_amdgcn_s_barrier(); asm volatile("" ::: "memory"); } while (0)
; #define G_SCHED __builtin_amdgcn_sched_barrier(0)
; #define STG_A(b, h, kt) do { const unsigned char* _g = A + (size_t)KT_(kt) * ASTEP; \
;         dma16((const void*)(_g + (size_t)((h) * 128) * ROWB), ROWB ? aoff[0][0] : aoff[h][0], lds_u + SA_(b, h) + dma0); \
;         dma16((const void*)(_g + (size_t)((h) * 128 + 64) * ROWB), ROWB ? aoff[0][0] : aoff[h][1], lds_u + SA_(b, h) + dma1); } while (0)
; #define STG_B(b, h, kt) do { const unsigned char* _g = img + (size_t)KT_(kt) * 32768 + (h) * 16384; \
;         dma16((const void*)(_g + dma0), boffl, lds_u + SB_(b, h) + dma0); \
;         dma16((const void*)(_g + dma1), boffl, lds_u + SB_(b, h) + dma1); } while (0)
; #define LDA_(dst, b, h) do { _Pragma("unroll") for (int _m = 0; _m < 4; ++_m) { \
;         dst[_m].lo = *(LAS3 const i32x4d*)(ap0 + SA_(b, h) + _m * 2048); \
;         dst[_m].hi = *(LAS3 const i32x4d*)(ap1 + SA_(b, h) + _m * 2048); } } while (0)
;     ...
;     for (int t = 0; t < nt; t += 2) {
;         const int t1 = (t + 1 < nt) ? t + 1 : nt - 1, t2 = (t + 2 < nt) ? t + 2 : nt - 1, t3 = (t + 3 < nt) ? t + 3 : nt - 1;
;         LDBF(B0, 0, 0); G_SCHED; LDA_(At, 0, 0); STG_A(1, 1, t1);
;         G_WAIT_L(8); G_BAR; G_WAIT_L(0); MMAD(0, 0, At, B0); G_BAR; G_SCHED;
;         LDBF(B1, 0, 1); STG_B(0, 0, t2);
;         G_BAR; G_WAIT_L(0); MMAD(0, 1, At, B1); G_BAR;
;         LDA_(At, 0, 1); STG_A(0, 0, t2);
;         G_BAR; G_WAIT_L(0); MMAD(1, 0, At, B0); G_BAR; G_SCHED;
;         STG_B(0, 1, t2);
;         G_WAIT_V(6); G_BAR; MMAD(1, 1, At, B1); G_BAR;
;         LDBF(B0, 1, 0); G_SCHED; LDA_(At, 1, 0); STG_A(0, 1, t2);
;         G_WAIT_L(8); G_BAR; G_WAIT_L(0); MMAD(0, 0, At, B0); G_BAR; G_SCHED;
;         LDBF(B1, 1, 1); STG_B(1, 0, t3);
;         G_BAR; G_WAIT_L(0); MMAD(0, 1, At, B1); G_BAR;
;         LDA_(At, 1, 1); STG_A(1, 0, t3);
;         G_BAR; G_WAIT_L(0); MMAD(1, 0, At, B0); G_BAR; G_SCHED;
;         STG_B(1, 1, t3);
;         G_WAIT_V(6); G_BAR; MMAD(1, 1, At, B1); G_BAR;
	s_nop 0
	ds_read_b128 v[124:127], v139 offset:16384
	ds_read_b128 v[188:191], v139 offset:24576
	ds_read_b128 v[128:131], v140 offset:16384
	ds_read_b128 v[192:195], v140 offset:24576
	s_nop 0
	s_waitcnt vmcnt(8)
	s_barrier
	s_waitcnt lgkmcnt(0)
	s_setprio 1
	s_waitcnt lgkmcnt(1)
	v_mfma_scale_f32_16x16x128_f8f6f4 v[120:123], v[124:131], v[156:163], v[120:123], v144, v144 op_sel:[0,1,0] op_sel_hi:[0,0,0]
	s_waitcnt lgkmcnt(0)
	v_mfma_scale_f32_16x16x128_f8f6f4 v[112:115], v[188:195], v[156:163], v[112:115], v144, v144 op_sel:[0,1,0] op_sel_hi:[0,0,0]
	v_mfma_scale_f32_16x16x128_f8f6f4 v[104:107], v[124:131], v[164:171], v[104:107], v144, v144 op_sel:[0,1,0] op_sel_hi:[0,0,0]
	v_mfma_scale_f32_16x16x128_f8f6f4 v[164:167], v[188:195], v[164:171], v[96:99], v144, v144 op_sel:[0,1,0] op_sel_hi:[0,0,0]
	v_mfma_scale_f32_16x16x128_f8f6f4 v[168:171], v[124:131], v[172:179], v[88:91], v144, v144 op_sel:[0,1,0] op_sel_hi:[0,0,0]
	v_mfma_scale_f32_16x16x128_f8f6f4 v[172:175], v[188:195], v[172:179], v[80:83], v144, v144 op_sel:[0,1,0] op_sel_hi:[0,0,0]
	v_mfma_scale_f32_16x16x128_f8f6f4 v[176:179], v[124:131], v[180:187], v[76:79], v144, v144 op_sel:[0,1,0] op_sel_hi:[0,0,0]
	v_mfma_scale_f32_16x16x128_f8f6f4 v[180:183], v[188:195], v[180:187], v[72:75], v144, v144 op_sel:[0,1,0] op_sel_hi:[0,0,0]
	s_setprio 0
	s_barrier
	s_nop 4
	ds_read_b128 v[72:75], v137 offset:16384
	ds_read_b128 v[80:83], v137 offset:18432
	ds_read_b128 v[76:79], v138 offset:16384
	ds_read_b128 v[84:87], v138 offset:18432
	ds_read_b128 v[88:91], v137 offset:20480
	ds_read_b128 v[96:99], v137 offset:22528
	ds_read_b128 v[92:95], v138 offset:20480
	ds_read_b128 v[100:103], v138 offset:22528
	s_nop 0
	s_barrier
	s_waitcnt lgkmcnt(0)
	s_setprio 1
	s_waitcnt lgkmcnt(5)
	v_mfma_scale_f32_16x16x128_f8f6f4 v[68:71], v[0:7], v[72:79], v[68:71], v144, v144 op_sel:[0,1,0] op_sel_hi:[0,0,0]
	v_mfma_scale_f32_16x16x128_f8f6f4 v[64:67], v[148:155], v[72:79], v[64:67], v144, v144 op_sel:[0,1,0] op_sel_hi:[0,0,0]
	s_waitcnt lgkmcnt(4)
	v_mfma_scale_f32_16x16x128_f8f6f4 v[60:63], v[0:7], v[80:87], v[60:63], v144, v144 op_sel:[0,1,0] op_sel_hi:[0,0,0]
	v_mfma_scale_f32_16x16x128_f8f6f4 v[52:55], v[148:155], v[80:87], v[52:55], v144, v144 op_sel:[0,1,0] op_sel_hi:[0,0,0]
	s_waitcnt lgkmcnt(1)
	v_mfma_scale_f32_16x16x128_f8f6f4 v[216:219], v[0:7], v[88:95], v[44:47], v144, v144 op_sel:[0,1,0] op_sel_hi:[0,0,0]
	v_mfma_scale_f32_16x16x128_f8f6f4 v[220:223], v[148:155], v[88:95], v[40:43], v144, v144 op_sel:[0,1,0] op_sel_hi:[0,0,0]
	s_waitcnt lgkmcnt(0)
	v_mfma_scale_f32_16x16x128_f8f6f4 v[224:227], v[0:7], v[96:103], v[28:31], v144, v144 op_sel:[0,1,0] op_sel_hi:[0,0,0]
	v_mfma_scale_f32_16x16x128_f8f6f4 v[228:231], v[148:155], v[96:103], v[24:27], v144, v144 op_sel:[0,1,0] op_sel_hi:[0,0,0]
	s_setprio 0
	s_barrier
	v_readlane_b32 s71, v255, 9
	s_waitcnt vmcnt(4)
	s_barrier
	v_readlane_b32 s68, v255, 11
	s_setprio 1
	v_mfma_scale_f32_16x16x128_f8f6f4 v[56:59], v[124:131], v[72:79], v[56:59], v144, v144 op_sel:[0,1,0] op_sel_hi:[0,0,0]
	v_mfma_scale_f32_16x16x128_f8f6f4 v[48:51], v[188:195], v[72:79], v[48:51], v144, v144 op_sel:[0,1,0] op_sel_hi:[0,0,0]
	v_mfma_scale_f32_16x16x128_f8f6f4 v[232:235], v[124:131], v[80:87], v[36:39], v144, v144 op_sel:[0,1,0] op_sel_hi:[0,0,0]
	v_mfma_scale_f32_16x16x128_f8f6f4 v[236:239], v[188:195], v[80:87], v[32:35], v144, v144 op_sel:[0,1,0] op_sel_hi:[0,0,0]
	v_mfma_scale_f32_16x16x128_f8f6f4 v[240:243], v[124:131], v[88:95], v[20:23], v144, v144 op_sel:[0,1,0] op_sel_hi:[0,0,0]
	v_mfma_scale_f32_16x16x128_f8f6f4 v[244:247], v[188:195], v[88:95], v[16:19], v144, v144 op_sel:[0,1,0] op_sel_hi:[0,0,0]
	v_mfma_scale_f32_16x16x128_f8f6f4 v[248:251], v[124:131], v[96:103], v[12:15], v144, v144 op_sel:[0,1,0] op_sel_hi:[0,0,0]
	v_mfma_scale_f32_16x16x128_f8f6f4 v[188:191], v[188:195], v[96:103], v[8:11], v144, v144 op_sel:[0,1,0] op_sel_hi:[0,0,0]
	s_setprio 0
	s_barrier
	ds_read_b128 v[0:3], v139 offset:32768
	s_nop 3
	ds_read_b128 v[8:11], v139 offset:40960
	ds_read_b128 v[4:7], v140 offset:32768
	ds_read_b128 v[12:15], v140 offset:40960
	ds_read_b128 v[16:19], v137 offset:32768
	ds_read_b128 v[24:27], v137 offset:34816
	ds_read_b128 v[20:23], v138 offset:32768
	ds_read_b128 v[28:31], v138 offset:34816
	ds_read_b128 v[32:35], v137 offset:36864
	ds_read_b128 v[40:43], v137 offset:38912
	ds_read_b128 v[36:39], v138 offset:36864
	ds_read_b128 v[44:47], v138 offset:38912
	s_waitcnt lgkmcnt(8)
	s_waitcnt vmcnt(2)
	s_barrier
; #define G_WAIT_V(n) asm volatile("s_waitcnt vmcnt(" #n ")" ::: "memory")
; #define G_WAIT_L(n) asm volatile("s_waitcnt lgkmcnt(" #n ")" ::: "memory")
; #define G_BAR do { asm volatile("" ::: "memory"); __builtin_amdgcn_s_barrier(); asm volatile("" ::: "memory"); } while (0)
; #define G_SCHED __builtin_amdgcn_sched_barrier(0)
; #define STG_A(b, h, kt) do { const unsigned char* _g = A + (size_t)KT_(kt) * ASTEP; \
;         dma16((const void*)(_g + (size_t)((h) * 128) * ROWB), ROWB ? aoff[0][0] : aoff[h][0], lds_u + SA_(b, h) + dma0); \
;         dma16((const void*)(_g + (size_t)((h) * 128 + 64) * ROWB), ROWB ? aoff[0][0] : aoff[h][1], lds_u + SA_(b, h) + dma1); } while (0)
; #define STG_B(b, h, kt) do { const unsigned char* _g = img + (size_t)KT_(kt) * 32768 + (h) * 16384; \
;         dma16((const void*)(_g + dma0), boffl, lds_u + SB_(b, h) + dma0); \
;         dma16((const void*)(_g + dma1), boffl, lds_u + SB_(b, h) + dma1); } while (0)
; #define LDA_(dst, b, h) do { _Pragma("unroll") for (int _m = 0; _m < 4; ++_m) { \
;         dst[_m].lo = *(LAS3 const i32x4d*)(ap0 + SA_(b, h) + _m * 2048); \
;         dst[_m].hi = *(LAS3 const i32x4d*)(ap1 + SA_(b, h) + _m * 2048); } } while (0)
;     ...
;     for (int t = 0; t < nt; t += 2) {
;         const int t1 = (t + 1 < nt) ? t + 1 : nt - 1, t2 = (t + 2 < nt) ? t + 2 : nt - 1, t3 = (t + 3 < nt) ? t + 3 : nt - 1;
;         LDBF(B0, 0, 0); G_SCHED; LDA_(At, 0, 0); STG_A(1, 1, t1);
;         G_WAIT_L(8); G_BAR; G_WAIT_L(0); MMAD(0, 0, At, B0); G_BAR; G_SCHED;
;         LDBF(B1, 0, 1); STG_B(0, 0, t2);
;         G_BAR; G_WAIT_L(0); MMAD(0, 1, At, B1); G_BAR;
;         LDA_(At, 0, 1); STG_A(0, 0, t2);
;         G_BAR; G_WAIT_L(0); MMAD(1, 0, At, B0); G_BAR; G_SCHED;
;         STG_B(0, 1, t2);
;         G_WAIT_V(6); G_BAR; MMAD(1, 1, At, B1); G_BAR;
;         LDBF(B0, 1, 0); G_SCHED; LDA_(At, 1, 0); STG_A(0, 1, t2);
;         G_WAIT_L(8); G_BAR; G_WAIT_L(0); MMAD(0, 0, At, B0); G_BAR; G_SCHED;
;         LDBF(B1, 1, 1); STG_B(1, 0, t3);
;         G_BAR; G_WAIT_L(0); MMAD(0, 1, At, B1); G_BAR;
;         LDA_(At, 1, 1); STG_A(1, 0, t3);
;         G_BAR; G_WAIT_L(0); MMAD(1, 0, At, B0); G_BAR; G_SCHED;
;         STG_B(1, 1, t3);
;         G_WAIT_V(6); G_BAR; MMAD(1, 1, At, B1); G_BAR;
;     }
;     G_WAIT_V(0); G_WAIT_L(0);
;     { int wr0 = wid >> 2; asm volatile("" : "+s"(wr0)); if (wr0 == 0) G_BAR; }
;     G_BAR;
	s_waitcnt lgkmcnt(0)
	v_readlane_b32 s60, v255, 10
	s_setprio 1
	s_waitcnt lgkmcnt(5)
	v_mfma_scale_f32_16x16x128_f8f6f4 v[132:135], v[0:7], v[16:23], v[132:135], v144, v144 op_sel:[0,1,0] op_sel_hi:[0,0,0]
	v_mfma_scale_f32_16x16x128_f8f6f4 v[128:131], v[8:15], v[16:23], v[196:199], v144, v144 op_sel:[0,1,0] op_sel_hi:[0,0,0]
	s_waitcnt lgkmcnt(4)
	v_mfma_scale_f32_16x16x128_f8f6f4 v[124:127], v[0:7], v[24:31], v[200:203], v144, v144 op_sel:[0,1,0] op_sel_hi:[0,0,0]
	v_mfma_scale_f32_16x16x128_f8f6f4 v[116:119], v[8:15], v[24:31], v[116:119], v144, v144 op_sel:[0,1,0] op_sel_hi:[0,0,0]
	s_waitcnt lgkmcnt(1)
	v_mfma_scale_f32_16x16x128_f8f6f4 v[108:111], v[0:7], v[32:39], v[108:111], v144, v144 op_sel:[0,1,0] op_sel_hi:[0,0,0]
	v_mfma_scale_f32_16x16x128_f8f6f4 v[100:103], v[8:15], v[32:39], v[204:207], v144, v144 op_sel:[0,1,0] op_sel_hi:[0,0,0]
	s_waitcnt lgkmcnt(0)
	v_mfma_scale_f32_16x16x128_f8f6f4 v[92:95], v[0:7], v[40:47], v[208:211], v144, v144 op_sel:[0,1,0] op_sel_hi:[0,0,0]
	v_mfma_scale_f32_16x16x128_f8f6f4 v[84:87], v[8:15], v[40:47], v[212:215], v144, v144 op_sel:[0,1,0] op_sel_hi:[0,0,0]
	s_setprio 0
	s_barrier
	ds_read_b128 v[148:151], v139 offset:49152
	ds_read_b128 v[156:159], v139 offset:57344
	ds_read_b128 v[152:155], v140 offset:49152
	ds_read_b128 v[160:163], v140 offset:57344
	s_waitcnt vmcnt(0)
	s_barrier
	s_waitcnt lgkmcnt(0)
	s_setprio 1
	s_waitcnt lgkmcnt(1)
	v_mfma_scale_f32_16x16x128_f8f6f4 v[120:123], v[148:155], v[16:23], v[120:123], v144, v144 op_sel:[0,1,0] op_sel_hi:[0,0,0]
	s_waitcnt lgkmcnt(0)
	v_mfma_scale_f32_16x16x128_f8f6f4 v[112:115], v[156:163], v[16:23], v[112:115], v144, v144 op_sel:[0,1,0] op_sel_hi:[0,0,0]
	v_mfma_scale_f32_16x16x128_f8f6f4 v[104:107], v[148:155], v[24:31], v[104:107], v144, v144 op_sel:[0,1,0] op_sel_hi:[0,0,0]
	v_mfma_scale_f32_16x16x128_f8f6f4 v[96:99], v[156:163], v[24:31], v[164:167], v144, v144 op_sel:[0,1,0] op_sel_hi:[0,0,0]
	v_mfma_scale_f32_16x16x128_f8f6f4 v[88:91], v[148:155], v[32:39], v[168:171], v144, v144 op_sel:[0,1,0] op_sel_hi:[0,0,0]
	v_mfma_scale_f32_16x16x128_f8f6f4 v[80:83], v[156:163], v[32:39], v[172:175], v144, v144 op_sel:[0,1,0] op_sel_hi:[0,0,0]
	v_mfma_scale_f32_16x16x128_f8f6f4 v[76:79], v[148:155], v[40:47], v[176:179], v144, v144 op_sel:[0,1,0] op_sel_hi:[0,0,0]
	v_mfma_scale_f32_16x16x128_f8f6f4 v[72:75], v[156:163], v[40:47], v[180:183], v144, v144 op_sel:[0,1,0] op_sel_hi:[0,0,0]
	s_setprio 0
	s_barrier
	ds_read_b128 v[16:19], v137 offset:49152
	ds_read_b128 v[164:167], v137 offset:51200
	ds_read_b128 v[20:23], v138 offset:49152
	ds_read_b128 v[168:171], v138 offset:51200
	ds_read_b128 v[172:175], v137 offset:53248
	ds_read_b128 v[180:183], v137 offset:55296
	ds_read_b128 v[176:179], v138 offset:53248
	ds_read_b128 v[184:187], v138 offset:55296
	s_barrier
	s_waitcnt lgkmcnt(0)
	s_setprio 1
	s_waitcnt lgkmcnt(5)
	v_mfma_scale_f32_16x16x128_f8f6f4 v[68:71], v[0:7], v[16:23], v[68:71], v144, v144 op_sel:[0,1,0] op_sel_hi:[0,0,0]
	v_mfma_scale_f32_16x16x128_f8f6f4 v[64:67], v[8:15], v[16:23], v[64:67], v144, v144 op_sel:[0,1,0] op_sel_hi:[0,0,0]
	s_waitcnt lgkmcnt(4)
	v_mfma_scale_f32_16x16x128_f8f6f4 v[60:63], v[0:7], v[164:171], v[60:63], v144, v144 op_sel:[0,1,0] op_sel_hi:[0,0,0]
	v_mfma_scale_f32_16x16x128_f8f6f4 v[52:55], v[8:15], v[164:171], v[52:55], v144, v144 op_sel:[0,1,0] op_sel_hi:[0,0,0]
	s_waitcnt lgkmcnt(1)
	v_mfma_scale_f32_16x16x128_f8f6f4 v[44:47], v[0:7], v[172:179], v[216:219], v144, v144 op_sel:[0,1,0] op_sel_hi:[0,0,0]
	v_mfma_scale_f32_16x16x128_f8f6f4 v[40:43], v[8:15], v[172:179], v[220:223], v144, v144 op_sel:[0,1,0] op_sel_hi:[0,0,0]
	s_waitcnt lgkmcnt(0)
	v_mfma_scale_f32_16x16x128_f8f6f4 v[28:31], v[0:7], v[180:187], v[224:227], v144, v144 op_sel:[0,1,0] op_sel_hi:[0,0,0]
	v_mfma_scale_f32_16x16x128_f8f6f4 v[24:27], v[8:15], v[180:187], v[228:231], v144, v144 op_sel:[0,1,0] op_sel_hi:[0,0,0]
	s_setprio 0
	s_barrier
	s_waitcnt vmcnt(0)
	s_barrier
	s_setprio 1
	v_mfma_scale_f32_16x16x128_f8f6f4 v[56:59], v[148:155], v[16:23], v[56:59], v144, v144 op_sel:[0,1,0] op_sel_hi:[0,0,0]
	v_mfma_scale_f32_16x16x128_f8f6f4 v[48:51], v[156:163], v[16:23], v[48:51], v144, v144 op_sel:[0,1,0] op_sel_hi:[0,0,0]
	v_mfma_scale_f32_16x16x128_f8f6f4 v[36:39], v[148:155], v[164:171], v[232:235], v144, v144 op_sel:[0,1,0] op_sel_hi:[0,0,0]
	v_mfma_scale_f32_16x16x128_f8f6f4 v[32:35], v[156:163], v[164:171], v[236:239], v144, v144 op_sel:[0,1,0] op_sel_hi:[0,0,0]
	v_mfma_scale_f32_16x16x128_f8f6f4 v[20:23], v[148:155], v[172:179], v[240:243], v144, v144 op_sel:[0,1,0] op_sel_hi:[0,0,0]
	v_mfma_scale_f32_16x16x128_f8f6f4 v[16:19], v[156:163], v[172:179], v[244:247], v144, v144 op_sel:[0,1,0] op_sel_hi:[0,0,0]
	v_mfma_scale_f32_16x16x128_f8f6f4 v[12:15], v[148:155], v[180:187], v[248:251], v144, v144 op_sel:[0,1,0] op_sel_hi:[0,0,0]
	v_mfma_scale_f32_16x16x128_f8f6f4 v[8:11], v[156:163], v[180:187], v[188:191], v144, v144 op_sel:[0,1,0] op_sel_hi:[0,0,0]
	s_setprio 0
	s_barrier
	s_mov_b32 vcc_hi, vcc_lo
	s_waitcnt vmcnt(0)
	s_waitcnt lgkmcnt(0)
	s_mov_b32 s0, s38
	s_mov_b32 s72, s83
	s_mov_b32 s70, s82
	s_mov_b32 s61, s79
	s_mov_b32 s59, s89
	s_mov_b32 s77, s38
	s_cmp_eq_u32 s0, 0
	s_cbranch_scc0 .LBB0_565
	s_barrier
